# stacked: lane-parallel MoE expert lookup; ws/gridDim cached in SGPRs in GEMM unit loops; GEMM1/GEMM2 first K-trip peeled with C=0 (no accumulator zeroing); counted vmcnt for side-stream consume; GEMM1
# speedup vs baseline: 1.0251x; 1.0251x over previous
_Z6mk_fwd4Args:
	s_mov_b64 s[52:53], s[0:1]
	s_load_dwordx2 s[0:1], s[0:1], 0xc0
	v_readfirstlane_b32 s61, v0
	s_mov_b32 s50, s2
	s_waitcnt lgkmcnt(0)
	s_mov_b64 s[100:101], s[0:1]
	v_writelane_b32 v254, s0, 0
	s_nop 1
	v_writelane_b32 v254, s1, 1
	s_load_dword s0, s[52:53], 0xd0
	v_mbcnt_lo_u32_b32 v0, -1, 0
	v_mbcnt_hi_u32_b32 v0, -1, v0
	s_waitcnt lgkmcnt(0)
	s_mov_b32 s99, s0
	v_writelane_b32 v254, s0, 2
	s_add_u32 s0, s52, 0xd0
	s_addc_u32 s1, s53, 0
	s_and_b32 s33, s61, 0xffffffc0
	v_writelane_b32 v254, s0, 3
	v_add_u32_e32 v0, s33, v0
	v_cmp_gt_i32_e32 vcc, 32, v0
	v_writelane_b32 v254, s1, 4
	s_and_saveexec_b64 s[0:1], vcc
	v_lshl_add_u32 v1, v0, 2, 0
	v_add_u32_e32 v1, 0x24a00, v1
	v_mov_b32_e32 v2, 0
	ds_write_b32 v1, v2
	s_or_b64 exec, exec, s[0:1]
	s_load_dwordx2 s[0:1], s[52:53], 0xc8
	s_waitcnt lgkmcnt(0)
	s_barrier
	v_cmp_eq_u32_e32 vcc, 0, v0
	v_writelane_b32 v254, s0, 5
	s_nop 1
	v_writelane_b32 v254, s1, 6
	s_load_dwordx2 s[0:1], s[52:53], 0xc0
	s_waitcnt lgkmcnt(0)
	s_add_u32 s0, s0, 0x4000
	s_addc_u32 s1, s1, 0
	v_writelane_b32 v254, s0, 7
	s_nop 1
	v_writelane_b32 v254, s1, 8
	s_getreg_b32 s0, hwreg(HW_REG_XCC_ID, 0, 4)
	s_and_b32 s0, s0, 15
	v_writelane_b32 v254, s0, 9
	s_and_saveexec_b64 s[0:1], vcc
	s_cbranch_execz .LBB0_6
	s_mov_b64 s[4:5], exec
	v_mbcnt_lo_u32_b32 v0, s4, 0
	v_mbcnt_hi_u32_b32 v0, s5, v0
	v_cmp_eq_u32_e32 vcc, 0, v0
	s_and_saveexec_b64 s[2:3], vcc
	s_cbranch_execz .LBB0_5
	v_readlane_b32 s6, v254, 9
	s_bcnt1_i32_b64 s4, s[4:5]
	s_lshl_b32 s6, s6, 8
	v_mov_b32_e32 v2, s4
	v_readlane_b32 s4, v254, 7
	v_mov_b32_e32 v1, s6
	v_readlane_b32 s5, v254, 8
	s_nop 4
	global_atomic_add v1, v1, v2, s[4:5] offset:1024 sc0

.LBB0_237:
	v_readlane_b32 s0, v254, 13
	v_readlane_b32 s1, v254, 14
	s_mov_b32 s0, s99
	s_add_i32 s46, s47, 1
	s_waitcnt lgkmcnt(0)
	s_mul_i32 s4, s46, s0
	v_readlane_b32 s0, v254, 11
	s_add_i32 s4, s4, s0
	s_cmpk_lt_i32 s4, 0x600
	s_cselect_b64 s[0:1], -1, 0
	s_cmpk_gt_i32 s4, 0x5ff
	s_cselect_b64 s[76:77], -1, 0
	s_and_b64 vcc, exec, s[76:77]
	s_cbranch_vccnz .LBB0_239
	s_ashr_i32 s5, s4, 31
	s_lshr_b32 s5, s5, 29
	s_add_i32 s5, s4, s5
	s_ashr_i32 s8, s5, 3
	s_and_b32 s5, s5, -8
	s_sub_i32 s4, s4, s5
	s_cmp_lt_i32 s4, 0
	s_cselect_b32 s5, s69, 0xc0
	s_mul_i32 s4, s5, s4
	s_add_i32 s4, s4, s8
	s_mul_hi_i32 s5, s4, 0x2aaaaaab
	s_lshr_b32 s8, s5, 31
	s_ashr_i32 s5, s5, 4
	s_add_i32 s5, s5, s8
	s_lshl_b32 s8, s5, 3
	s_mulk_i32 s5, 0x60
	s_sub_i32 s4, s4, s5
	s_bfe_i32 s5, s4, 0x80000
	s_bfe_u32 s5, s5, 0x3000c
	s_add_i32 s5, s4, s5
	s_bfe_i32 s24, s5, 0x80000
	s_and_b32 s5, s5, 0xf8
	s_sub_i32 s4, s4, s5
	s_sext_i32_i16 s24, s24
	s_sext_i32_i8 s4, s4
	s_add_i32 s45, s8, s4
	s_ashr_i32 s74, s24, 3
.LBB0_239:
	v_cndmask_b32_e64 v128, 0, 1, s[0:1]
	v_cmp_ne_u32_e64 s[4:5], 1, v128
	s_andn2_b64 vcc, exec, s[0:1]
	s_mov_b64 s[78:79], s[6:7]
	s_cbranch_vccnz .LBB0_241
	v_readlane_b32 s24, v254, 13
	v_readlane_b32 s25, v254, 14
	s_mov_b64 s[24:25], s[100:101]
	s_ashr_i32 s75, s74, 31
	s_lshl_b64 s[34:35], s[74:75], 20
	s_waitcnt lgkmcnt(0)
	s_add_u32 s8, s24, s34
	s_addc_u32 s24, s25, s35
	s_add_u32 s78, s8, 0x400000
	s_addc_u32 s79, s24, 0

.LBB0_249:
	v_readlane_b32 s0, v254, 13
	v_readlane_b32 s1, v254, 14
	v_mbcnt_lo_u32_b32 v165, -1, 0
	v_mbcnt_hi_u32_b32 v165, -1, v165
	s_mov_b64 s[6:7], s[100:101]
	s_cmp_lt_i32 s83, 8
	s_cselect_b64 s[0:1], -1, 0
	s_cmp_gt_i32 s83, 7
	v_mov_b32_e32 v180, v96
	v_mov_b32_e32 v181, v97
	v_mov_b32_e32 v182, v98
	v_mov_b32_e32 v183, v99
	v_mov_b32_e32 v167, v100
	v_mov_b32_e32 v169, v101
	v_mov_b32_e32 v171, v102
	v_mov_b32_e32 v179, v103
	s_cbranch_scc1 .LBB0_251
	v_and_b32_e32 v173, 0x7fffffff, v101
	v_and_b32_e32 v172, 0x7fffffff, v100
	v_pk_fma_f32 v[172:173], v[172:173], s[56:57], 1.0 op_sel_hi:[1,0,0]
	v_mov_b64_e32 v[174:175], s[60:61]
	v_rcp_f32_e32 v172, v172
	v_rcp_f32_e32 v173, v173
	v_pk_mul_f32 v[182:183], v[100:101], v[100:101]
	v_cmp_gt_f32_e32 vcc, 0, v100
	v_pk_mul_f32 v[182:183], v[182:183], s[68:69] op_sel_hi:[1,0]
	v_pk_fma_f32 v[180:181], v[172:173], s[58:59], v[174:175] op_sel_hi:[1,0,0]
	v_exp_f32_e32 v182, v182
	v_pk_fma_f32 v[180:181], v[172:173], v[180:181], s[62:63] op_sel_hi:[1,1,0]
	v_exp_f32_e32 v183, v183
	v_pk_fma_f32 v[180:181], v[172:173], v[180:181], s[64:65] op_sel_hi:[1,1,0]
	s_nop 0
	v_pk_fma_f32 v[180:181], v[172:173], v[180:181], s[66:67] op_sel_hi:[1,1,0]
	s_nop 0
	v_pk_mul_f32 v[172:173], v[172:173], v[180:181]
	v_pk_mul_f32 v[180:181], v[102:103], v[102:103]
	v_pk_mul_f32 v[172:173], v[182:183], v[172:173]
	v_pk_mul_f32 v[180:181], v[180:181], s[68:69] op_sel_hi:[1,0]
	v_pk_mul_f32 v[182:183], v[100:101], v[172:173]
	v_pk_fma_f32 v[172:173], v[100:101], v[172:173], v[100:101] neg_lo:[1,0,0] neg_hi:[1,0,0]
	v_exp_f32_e32 v180, v180
	v_cndmask_b32_e32 v167, v172, v182, vcc
	v_cmp_gt_f32_e32 vcc, 0, v101
	v_and_b32_e32 v172, 0x7fffffff, v102
	v_exp_f32_e32 v181, v181
	v_cndmask_b32_e32 v169, v173, v183, vcc
	v_and_b32_e32 v173, 0x7fffffff, v103
	v_pk_fma_f32 v[172:173], v[172:173], s[56:57], 1.0 op_sel_hi:[1,0,0]
	v_cmp_gt_f32_e32 vcc, 0, v102
	v_rcp_f32_e32 v172, v172
	v_rcp_f32_e32 v173, v173
	s_nop 0
	v_pk_fma_f32 v[182:183], v[172:173], s[58:59], v[174:175] op_sel_hi:[1,0,0]
	s_nop 0
	v_pk_fma_f32 v[182:183], v[172:173], v[182:183], s[62:63] op_sel_hi:[1,1,0]
	s_nop 0
	v_pk_fma_f32 v[182:183], v[172:173], v[182:183], s[64:65] op_sel_hi:[1,1,0]
	s_nop 0
	v_pk_fma_f32 v[182:183], v[172:173], v[182:183], s[66:67] op_sel_hi:[1,1,0]
	s_nop 0
	v_pk_mul_f32 v[172:173], v[172:173], v[182:183]
	v_pk_mul_f32 v[182:183], v[98:99], v[98:99]
	v_pk_mul_f32 v[172:173], v[180:181], v[172:173]
	s_nop 0
	v_pk_mul_f32 v[180:181], v[102:103], v[172:173]
	v_pk_fma_f32 v[172:173], v[102:103], v[172:173], v[102:103] neg_lo:[1,0,0] neg_hi:[1,0,0]
	s_nop 0
	v_cndmask_b32_e32 v171, v172, v180, vcc
	v_cmp_gt_f32_e32 vcc, 0, v103
	v_and_b32_e32 v172, 0x7fffffff, v96
	s_nop 0
	v_cndmask_b32_e32 v179, v173, v181, vcc
	v_and_b32_e32 v173, 0x7fffffff, v97
	v_pk_fma_f32 v[172:173], v[172:173], s[56:57], 1.0 op_sel_hi:[1,0,0]
	v_cmp_gt_f32_e32 vcc, 0, v96
	v_rcp_f32_e32 v172, v172
	v_rcp_f32_e32 v173, v173
	s_nop 0
	v_pk_fma_f32 v[180:181], v[172:173], s[58:59], v[174:175] op_sel_hi:[1,0,0]
	s_nop 0
	v_pk_fma_f32 v[180:181], v[172:173], v[180:181], s[62:63] op_sel_hi:[1,1,0]
	s_nop 0
	v_pk_fma_f32 v[180:181], v[172:173], v[180:181], s[64:65] op_sel_hi:[1,1,0]
	s_nop 0
	v_pk_fma_f32 v[180:181], v[172:173], v[180:181], s[66:67] op_sel_hi:[1,1,0]
	s_nop 0
	v_pk_mul_f32 v[172:173], v[172:173], v[180:181]
	v_pk_mul_f32 v[180:181], v[96:97], v[96:97]
	s_nop 0
	v_pk_mul_f32 v[180:181], v[180:181], s[68:69] op_sel_hi:[1,0]
	s_nop 0
	v_exp_f32_e32 v180, v180
	v_exp_f32_e32 v181, v181
	s_nop 0
	v_pk_mul_f32 v[172:173], v[180:181], v[172:173]
	s_nop 0
	v_pk_mul_f32 v[180:181], v[96:97], v[172:173]
	v_pk_fma_f32 v[172:173], v[96:97], v[172:173], v[96:97] neg_lo:[1,0,0] neg_hi:[1,0,0]
	s_nop 0
	v_cndmask_b32_e32 v180, v172, v180, vcc
	v_cmp_gt_f32_e32 vcc, 0, v97
	v_and_b32_e32 v172, 0x7fffffff, v98
	s_nop 0
	v_cndmask_b32_e32 v181, v173, v181, vcc
	v_and_b32_e32 v173, 0x7fffffff, v99
	v_pk_fma_f32 v[172:173], v[172:173], s[56:57], 1.0 op_sel_hi:[1,0,0]
	v_cmp_gt_f32_e32 vcc, 0, v98
	v_rcp_f32_e32 v172, v172
	v_rcp_f32_e32 v173, v173
	s_nop 0
	v_pk_fma_f32 v[174:175], v[172:173], s[58:59], v[174:175] op_sel_hi:[1,0,0]
	s_nop 0
	v_pk_fma_f32 v[174:175], v[172:173], v[174:175], s[62:63] op_sel_hi:[1,1,0]
	s_nop 0
	v_pk_fma_f32 v[174:175], v[172:173], v[174:175], s[64:65] op_sel_hi:[1,1,0]
	s_nop 0
	v_pk_fma_f32 v[174:175], v[172:173], v[174:175], s[66:67] op_sel_hi:[1,1,0]
	s_nop 0
	v_pk_mul_f32 v[172:173], v[172:173], v[174:175]
	v_pk_mul_f32 v[174:175], v[182:183], s[68:69] op_sel_hi:[1,0]
	s_nop 0
	v_exp_f32_e32 v174, v174
	v_exp_f32_e32 v175, v175
	s_nop 0
	v_pk_mul_f32 v[172:173], v[174:175], v[172:173]
	s_nop 0
	v_pk_mul_f32 v[174:175], v[98:99], v[172:173]
	v_pk_fma_f32 v[172:173], v[98:99], v[172:173], v[98:99] neg_lo:[1,0,0] neg_hi:[1,0,0]
	s_nop 0
	v_cndmask_b32_e32 v182, v172, v174, vcc
	v_cmp_gt_f32_e32 vcc, 0, v99
	s_nop 1
	v_cndmask_b32_e32 v183, v173, v175, vcc

.LBB0_281:
	v_cvt_pk_bf16_f32 v180, v163, v165
	v_cvt_pk_bf16_f32 v181, v167, v169
	s_nop 0
	v_cvt_pk_bf16_f32 v182, v171, v174
	v_cvt_pk_bf16_f32 v183, v175, v179
	global_store_dwordx4 v[172:173], v[180:183], off offset:16
	s_add_u32 s0, s75, 0xffffff00
	s_addc_u32 s1, s48, -1
	s_waitcnt vmcnt(16)
	v_mul_f32_e32 v128, 0x43800000, v128
	v_mul_f32_e32 v132, 0x43800000, v132
	v_mov_b32_e32 v180, v161
	v_cvt_pk_fp8_f32 v180, v128, v132
	v_mul_f32_e32 v128, 0x43800000, v144
	v_mul_f32_e32 v132, 0x43800000, v148
	v_mov_b32_e32 v181, v161
	v_cvt_pk_fp8_f32 v181, v128, v132
	v_mul_f32_e32 v128, 0x43800000, v152
	v_mul_f32_e32 v132, 0x43800000, v156
	v_mul_f32_e32 v129, 0x43800000, v129
	v_cvt_pk_fp8_f32 v181, v128, v132 op_sel:[0,0,1]
	v_mul_f32_e32 v132, 0x43800000, v133
	v_mov_b32_e32 v128, v161
	v_mul_f32_e32 v133, 0x43800000, v137
	v_cvt_pk_fp8_f32 v128, v129, v132
	v_mul_f32_e32 v132, 0x43800000, v145
	v_mul_f32_e32 v137, 0x43800000, v149
	v_mov_b32_e32 v129, v161
	v_cvt_pk_fp8_f32 v129, v132, v137
	v_mul_f32_e32 v136, 0x43800000, v136
	v_mul_f32_e32 v140, 0x43800000, v140
	v_cvt_pk_fp8_f32 v180, v136, v140 op_sel:[0,0,1]
	v_mul_f32_e32 v136, 0x43800000, v141
	v_cvt_pk_fp8_f32 v128, v133, v136 op_sel:[0,0,1]
	v_mul_f32_e32 v132, 0x43800000, v153
	v_mul_f32_e32 v133, 0x43800000, v157
	s_lshl_b32 s6, s24, 6
	s_lshr_b32 s7, s24, 3
	v_cvt_pk_fp8_f32 v129, v132, v133 op_sel:[0,0,1]
	v_mul_f32_e32 v130, 0x43800000, v130
	v_mul_f32_e32 v133, 0x43800000, v134
	v_mov_b32_e32 v132, v161
	s_and_b32 s6, s6, 0xfc0
	s_and_b32 s7, s7, 8
	v_cvt_pk_fp8_f32 v132, v130, v133
	v_mul_f32_e32 v130, 0x43800000, v146
	v_mul_f32_e32 v137, 0x43800000, v150
	v_mov_b32_e32 v133, v161
	s_or_b32 s34, s6, s7
	v_readlane_b32 s6, v254, 13
	v_cvt_pk_fp8_f32 v133, v130, v137
	v_readlane_b32 s7, v254, 14
	v_mbcnt_lo_u32_b32 v163, -1, 0
	v_mbcnt_hi_u32_b32 v163, -1, v163
	v_mul_f32_e32 v134, 0x43800000, v138
	v_mul_f32_e32 v136, 0x43800000, v142
	s_mov_b64 s[6:7], s[100:101]
	v_cvt_pk_fp8_f32 v132, v134, v136 op_sel:[0,0,1]
	v_mul_f32_e32 v130, 0x43800000, v154
	v_mul_f32_e32 v134, 0x43800000, v158
	s_lshl_b64 s[24:25], s[80:81], 12
	v_lshlrev_b32_e32 v165, 3, v163
	v_lshlrev_b32_e32 v167, 2, v163
	v_cvt_pk_fp8_f32 v133, v130, v134 op_sel:[0,0,1]
	v_mul_f32_e32 v131, 0x43800000, v131
	v_mul_f32_e32 v134, 0x43800000, v135
	v_mov_b32_e32 v130, v161
	s_or_b32 s24, s24, s34
	v_and_b32_e32 v165, 48, v165
	v_and_b32_e32 v167, 4, v167
	v_cvt_pk_fp8_f32 v130, v131, v134
	v_mul_f32_e32 v134, 0x43800000, v147
	v_mul_f32_e32 v137, 0x43800000, v151
	v_mov_b32_e32 v131, v161
	v_or3_b32 v172, s24, v165, v167
	v_mov_b32_e32 v173, s25
	v_cvt_pk_fp8_f32 v131, v134, v137
	v_lshlrev_b64 v[172:173], 11, v[172:173]
	s_waitcnt lgkmcnt(0)
	v_lshl_add_u64 v[172:173], s[6:7], 0, v[172:173]
	v_and_b32_e32 v174, -8, v163
	v_mul_f32_e32 v135, 0x43800000, v139
	v_mul_f32_e32 v136, 0x43800000, v143
	v_lshl_add_u64 v[172:173], v[172:173], 0, s[8:9]
	v_ashrrev_i32_e32 v175, 31, v174
	v_cvt_pk_fp8_f32 v130, v135, v136 op_sel:[0,0,1]
	v_mul_f32_e32 v134, 0x43800000, v155
	v_mul_f32_e32 v135, 0x43800000, v159
	v_lshl_add_u64 v[172:173], v[172:173], 0, v[174:175]
	v_cvt_pk_fp8_f32 v131, v134, v135 op_sel:[0,0,1]
	v_lshl_add_u64 v[174:175], v[172:173], 0, s[12:13]
	v_add_co_u32_e32 v172, vcc, s95, v172
	s_nop 1
	v_addc_co_u32_e32 v173, vcc, 0, v173, vcc
	s_and_b64 vcc, exec, s[4:5]
	global_store_dwordx2 v[172:173], v[180:181], off offset:-4096
	global_store_dwordx2 v[174:175], v[128:129], off offset:2048
	global_store_dwordx2 v[172:173], v[132:133], off
	global_store_dwordx2 v[172:173], v[130:131], off offset:2048
	s_cbranch_vccnz .LBB0_285
	s_and_b64 vcc, exec, s[2:3]
	s_cbranch_vccnz .LBB0_284
	s_barrier

.LBB0_625:
	v_readlane_b32 s2, v254, 13
	v_readlane_b32 s3, v254, 14
	s_mov_b32 s2, s99
	s_add_i32 s58, s56, 1
	v_readlane_b32 s3, v254, 11
	s_waitcnt lgkmcnt(0)
	s_mul_i32 s2, s58, s2
	s_add_i32 s2, s2, s3
	s_cmpk_lt_i32 s2, 0x400
	s_cselect_b64 s[34:35], -1, 0
	s_cmpk_gt_i32 s2, 0x3ff
	s_cselect_b64 s[28:29], -1, 0
	s_and_b64 vcc, exec, s[28:29]
	s_cbranch_vccnz .LBB0_631
	s_ashr_i32 s3, s2, 31
	s_lshr_b32 s3, s3, 29
	s_add_i32 s9, s2, s3
	s_and_b32 s3, s9, -8
	s_sub_i32 s26, s2, s3
	s_cmp_gt_i32 s26, -1
	s_mov_b64 s[2:3], -1
	s_cbranch_scc0 .LBB0_628
	s_lshl_b32 s27, s26, 7
	s_mov_b64 s[2:3], 0

.LBB0_631:
	v_cndmask_b32_e64 v128, 0, 1, s[34:35]
	v_cmp_ne_u32_e64 s[2:3], 1, v128
	s_andn2_b64 vcc, exec, s[34:35]
	s_mov_b64 s[30:31], s[36:37]
	s_cbranch_vccnz .LBB0_633
	v_readlane_b32 s30, v254, 13
	v_readlane_b32 s31, v254, 14
	s_mov_b64 s[30:31], s[100:101]
	s_ashr_i32 s27, s26, 31
	s_lshl_b64 s[38:39], s[26:27], 20
	s_waitcnt lgkmcnt(0)
	s_add_u32 s9, s30, s38
	s_addc_u32 s27, s31, s39
	s_add_u32 s30, s9, 0x1000000
	s_addc_u32 s31, s27, 0
.LBB0_633:
	s_cmp_lt_i32 s56, 1
	s_cbranch_scc1 .LBB0_636
	s_andn2_b64 vcc, exec, s[4:5]
	v_mbcnt_lo_u32_b32 v128, -1, 0
	v_mbcnt_hi_u32_b32 v128, -1, v128
	s_cbranch_vccnz .LBB0_636
	v_readlane_b32 s38, v254, 13
	v_readlane_b32 s39, v254, 14
	s_mov_b64 s[38:39], s[100:101]
	v_lshlrev_b32_e32 v128, 4, v128
	v_ashrrev_i32_e32 v129, 31, v128
	s_waitcnt lgkmcnt(0)
	s_add_u32 s27, s38, s43
	s_addc_u32 s40, s39, 0
	s_ashr_i32 s9, s8, 31
	s_lshl_b64 s[38:39], s[8:9], 10
	s_add_u32 s38, s27, s38
	s_addc_u32 s39, s40, s39
	s_bitcmp1_b32 s56, 0
	s_cselect_b32 s9, s51, 0x24c00
	v_lshl_add_u64 v[128:129], s[38:39], 0, v[128:129]
	s_add_i32 m0, s9, s42
	s_nop 0
	global_load_lds_dwordx4 v[128:129], off

.LBB0_644:
	v_readlane_b32 s36, v254, 13
	v_readlane_b32 s37, v254, 14
	v_mbcnt_lo_u32_b32 v128, -1, 0
	v_mbcnt_hi_u32_b32 v128, -1, v128
	s_add_u32 s34, s27, 0xffffff00
	s_load_dwordx2 s[38:39], s[36:37], 0x0
	s_nop 0
	s_mov_b64 s[36:37], s[100:101]
	s_addc_u32 s35, s59, -1
	s_lshl_b32 s27, s8, 8
	s_lshl_b32 s40, s10, 8
	s_add_i32 s27, s27, s47
	s_or_b32 s40, s40, s48
	v_and_b32_e32 v159, 15, v128
	v_and_b32_e32 v128, -16, v128
	s_cmp_gt_i32 s8, 63
	v_add_u32_e32 v168, s40, v128
	s_cselect_b32 s40, 0xc000, 0
	s_waitcnt lgkmcnt(0)
	s_add_u32 s40, s36, s40
	v_ashrrev_i32_e32 v169, 31, v168
	s_addc_u32 s41, s37, 0
	v_lshlrev_b64 v[144:145], 2, v[168:169]
	v_or_b32_e32 v172, s27, v159
	v_lshl_add_u64 v[128:129], s[40:41], 0, v[144:145]
	v_ashrrev_i32_e32 v173, 31, v172
	v_lshl_add_u64 v[136:137], v[128:129], 0, s[22:23]
	v_add_co_u32_e32 v128, vcc, s55, v128
	v_lshl_add_u64 v[170:171], s[38:39], 0, v[144:145]
	v_lshlrev_b64 v[144:145], 13, v[172:173]
	v_or_b32_e32 v230, 16, v172
	v_addc_co_u32_e32 v129, vcc, 0, v129, vcc
	v_lshl_add_u64 v[144:145], v[170:171], 0, v[144:145]
	v_ashrrev_i32_e32 v231, 31, v230
	global_load_dwordx4 v[140:143], v[128:129], off
	s_nop 0
	global_load_dwordx4 v[128:131], v[136:137], off offset:48
	global_load_dwordx4 v[132:135], v[136:137], off offset:32
	s_nop 0
	global_load_dwordx4 v[136:139], v[136:137], off offset:16
	s_nop 0
	global_load_dwordx4 v[178:181], v[144:145], off offset:48
	global_load_dwordx4 v[182:185], v[144:145], off offset:32
	global_load_dwordx4 v[186:189], v[144:145], off offset:16
	global_load_dwordx4 v[190:193], v[144:145], off
	v_lshlrev_b64 v[144:145], 13, v[230:231]
	v_or_b32_e32 v232, 32, v172
	v_lshl_add_u64 v[144:145], v[170:171], 0, v[144:145]
	v_ashrrev_i32_e32 v233, 31, v232
	global_load_dwordx4 v[194:197], v[144:145], off offset:48
	global_load_dwordx4 v[198:201], v[144:145], off offset:32
	global_load_dwordx4 v[202:205], v[144:145], off offset:16
	global_load_dwordx4 v[206:209], v[144:145], off
	v_lshlrev_b64 v[144:145], 13, v[232:233]
	v_or_b32_e32 v234, 48, v172
	v_lshl_add_u64 v[144:145], v[170:171], 0, v[144:145]
	v_ashrrev_i32_e32 v235, 31, v234
	global_load_dwordx4 v[210:213], v[144:145], off offset:48
	global_load_dwordx4 v[214:217], v[144:145], off offset:32
	global_load_dwordx4 v[218:221], v[144:145], off offset:16
	global_load_dwordx4 v[222:225], v[144:145], off
	v_lshlrev_b64 v[144:145], 13, v[234:235]
	v_lshl_add_u64 v[226:227], v[170:171], 0, v[144:145]
	global_load_dwordx4 v[144:147], v[226:227], off offset:48
	global_load_dwordx4 v[148:151], v[226:227], off offset:32
	global_load_dwordx4 v[152:155], v[226:227], off offset:16
	s_nop 0
	global_load_dwordx4 v[226:229], v[226:227], off
	s_lshl_b32 s27, s47, 2
	s_add_i32 s9, s9, s27
	v_lshl_add_u32 v159, v159, 2, s9
	ds_read_b32 v236, v159
	v_lshl_add_u64 v[168:169], v[168:169], 1, s[36:37]
	v_lshlrev_b64 v[238:239], 12, v[172:173]
	v_lshl_add_u64 v[168:169], v[168:169], 0, s[24:25]
	v_lshl_add_u64 v[238:239], v[168:169], 0, v[238:239]
	s_waitcnt lgkmcnt(0)
	v_pk_mul_f32 v[248:249], v[52:53], v[236:237] op_sel_hi:[1,0]
	v_pk_mul_f32 v[250:251], v[54:55], v[236:237] op_sel_hi:[1,0]
	v_pk_mul_f32 v[240:241], v[100:101], v[236:237] op_sel_hi:[1,0]
	v_pk_mul_f32 v[242:243], v[102:103], v[236:237] op_sel_hi:[1,0]
	v_pk_mul_f32 v[244:245], v[96:97], v[236:237] op_sel_hi:[1,0]
	v_pk_mul_f32 v[246:247], v[98:99], v[236:237] op_sel_hi:[1,0]
	v_pk_mul_f32 v[252:253], v[44:45], v[236:237] op_sel_hi:[1,0]
	v_pk_mul_f32 v[236:237], v[46:47], v[236:237] op_sel_hi:[1,0]
	s_waitcnt vmcnt(0)
	v_pk_fma_f32 v[184:185], v[134:135], v[250:251], v[184:185]
	v_pk_fma_f32 v[182:183], v[132:133], v[248:249], v[182:183]
	v_pk_fma_f32 v[192:193], v[142:143], v[242:243], v[192:193]
	v_pk_fma_f32 v[190:191], v[140:141], v[240:241], v[190:191]
	v_pk_fma_f32 v[188:189], v[138:139], v[246:247], v[188:189]
	v_pk_fma_f32 v[186:187], v[136:137], v[244:245], v[186:187]
	v_pk_fma_f32 v[236:237], v[130:131], v[236:237], v[180:181]
	v_pk_fma_f32 v[240:241], v[128:129], v[252:253], v[178:179]
	v_cvt_pk_bf16_f32 v178, v190, v191
	v_cvt_pk_bf16_f32 v179, v192, v193
	v_cvt_pk_bf16_f32 v180, v186, v187
	v_cvt_pk_bf16_f32 v181, v188, v189
	v_cvt_pk_bf16_f32 v182, v182, v183
	global_store_dwordx4 v[238:239], v[178:181], off
	v_cvt_pk_bf16_f32 v183, v184, v185
	v_cvt_pk_bf16_f32 v184, v240, v241
	v_cvt_pk_bf16_f32 v185, v236, v237
	global_store_dwordx4 v[238:239], v[182:185], off offset:16
	ds_read_b32 v182, v159 offset:64
	v_lshlrev_b64 v[178:179], 12, v[230:231]
	v_lshl_add_u64 v[184:185], v[168:169], 0, v[178:179]
	s_waitcnt lgkmcnt(0)
	v_pk_mul_f32 v[178:179], v[92:93], v[182:183] op_sel_hi:[1,0]
	v_pk_mul_f32 v[180:181], v[94:95], v[182:183] op_sel_hi:[1,0]
	v_pk_fma_f32 v[178:179], v[140:141], v[178:179], v[206:207]
	v_pk_fma_f32 v[180:181], v[142:143], v[180:181], v[208:209]
	v_pk_mul_f32 v[186:187], v[88:89], v[182:183] op_sel_hi:[1,0]
	v_pk_mul_f32 v[188:189], v[90:91], v[182:183] op_sel_hi:[1,0]
	v_pk_fma_f32 v[186:187], v[136:137], v[186:187], v[202:203]
	v_pk_fma_f32 v[188:189], v[138:139], v[188:189], v[204:205]
	v_cvt_pk_bf16_f32 v178, v178, v179
	v_cvt_pk_bf16_f32 v179, v180, v181
	v_cvt_pk_bf16_f32 v180, v186, v187
	v_pk_mul_f32 v[186:187], v[28:29], v[182:183] op_sel_hi:[1,0]
	v_cvt_pk_bf16_f32 v181, v188, v189
	global_store_dwordx4 v[184:185], v[178:181], off
	v_pk_fma_f32 v[186:187], v[128:129], v[186:187], v[194:195]
	s_nop 0
	v_pk_mul_f32 v[178:179], v[36:37], v[182:183] op_sel_hi:[1,0]
	v_pk_mul_f32 v[180:181], v[38:39], v[182:183] op_sel_hi:[1,0]
	v_pk_fma_f32 v[178:179], v[132:133], v[178:179], v[198:199]
	v_pk_fma_f32 v[180:181], v[134:135], v[180:181], v[200:201]
	v_pk_mul_f32 v[182:183], v[30:31], v[182:183] op_sel_hi:[1,0]
	v_cvt_pk_bf16_f32 v178, v178, v179
	v_cvt_pk_bf16_f32 v179, v180, v181
	v_cvt_pk_bf16_f32 v180, v186, v187
	s_nop 0
	v_pk_fma_f32 v[182:183], v[130:131], v[182:183], v[196:197]
	s_nop 0
	v_cvt_pk_bf16_f32 v181, v182, v183
	global_store_dwordx4 v[184:185], v[178:181], off offset:16
	ds_read_b32 v182, v159 offset:128
	s_nop 0
	v_lshlrev_b64 v[178:179], 12, v[232:233]
	v_lshl_add_u64 v[184:185], v[168:169], 0, v[178:179]
	s_waitcnt lgkmcnt(0)
	v_pk_mul_f32 v[178:179], v[84:85], v[182:183] op_sel_hi:[1,0]
	v_pk_mul_f32 v[180:181], v[86:87], v[182:183] op_sel_hi:[1,0]
	v_pk_fma_f32 v[178:179], v[140:141], v[178:179], v[222:223]
	v_pk_fma_f32 v[180:181], v[142:143], v[180:181], v[224:225]
	v_pk_mul_f32 v[186:187], v[76:77], v[182:183] op_sel_hi:[1,0]
	v_pk_mul_f32 v[188:189], v[78:79], v[182:183] op_sel_hi:[1,0]
	v_pk_fma_f32 v[186:187], v[136:137], v[186:187], v[218:219]
	v_pk_fma_f32 v[188:189], v[138:139], v[188:189], v[220:221]
	v_cvt_pk_bf16_f32 v178, v178, v179
	v_cvt_pk_bf16_f32 v179, v180, v181
	v_cvt_pk_bf16_f32 v180, v186, v187
	v_pk_mul_f32 v[186:187], v[12:13], v[182:183] op_sel_hi:[1,0]
	v_cvt_pk_bf16_f32 v181, v188, v189
	global_store_dwordx4 v[184:185], v[178:181], off
	v_pk_fma_f32 v[186:187], v[128:129], v[186:187], v[210:211]
	s_nop 0
	v_pk_mul_f32 v[178:179], v[20:21], v[182:183] op_sel_hi:[1,0]
	v_pk_mul_f32 v[180:181], v[22:23], v[182:183] op_sel_hi:[1,0]
	v_pk_fma_f32 v[178:179], v[132:133], v[178:179], v[214:215]
	v_pk_fma_f32 v[180:181], v[134:135], v[180:181], v[216:217]
	v_pk_mul_f32 v[182:183], v[14:15], v[182:183] op_sel_hi:[1,0]
	v_cvt_pk_bf16_f32 v178, v178, v179
	v_cvt_pk_bf16_f32 v179, v180, v181
	v_cvt_pk_bf16_f32 v180, v186, v187
	s_nop 0
	v_pk_fma_f32 v[182:183], v[130:131], v[182:183], v[212:213]
	s_nop 0
	v_cvt_pk_bf16_f32 v181, v182, v183
	global_store_dwordx4 v[184:185], v[178:181], off offset:16
	ds_read_b32 v178, v159 offset:192
	s_nop 0
	v_lshlrev_b64 v[180:181], 12, v[234:235]
	v_lshl_add_u64 v[180:181], v[168:169], 0, v[180:181]
	s_waitcnt lgkmcnt(0)
	v_pk_mul_f32 v[186:187], v[60:61], v[178:179] op_sel_hi:[1,0]
	v_pk_mul_f32 v[188:189], v[62:63], v[178:179] op_sel_hi:[1,0]
	v_pk_mul_f32 v[182:183], v[68:69], v[178:179] op_sel_hi:[1,0]
	v_pk_mul_f32 v[184:185], v[70:71], v[178:179] op_sel_hi:[1,0]
	v_pk_fma_f32 v[188:189], v[138:139], v[188:189], v[154:155]
	v_pk_fma_f32 v[154:155], v[136:137], v[186:187], v[152:153]
	v_pk_fma_f32 v[184:185], v[142:143], v[184:185], v[228:229]
	v_pk_fma_f32 v[182:183], v[140:141], v[182:183], v[226:227]
	v_cvt_pk_bf16_f32 v153, v184, v185
	v_cvt_pk_bf16_f32 v154, v154, v155
	v_cvt_pk_bf16_f32 v155, v188, v189
	s_nop 0
	v_cvt_pk_bf16_f32 v152, v182, v183
	global_store_dwordx4 v[180:181], v[152:155], off
	s_nop 1
	v_pk_mul_f32 v[152:153], v[8:9], v[178:179] op_sel_hi:[1,0]
	v_pk_mul_f32 v[154:155], v[10:11], v[178:179] op_sel_hi:[1,0]
	v_pk_fma_f32 v[148:149], v[132:133], v[152:153], v[148:149]
	v_pk_fma_f32 v[150:151], v[134:135], v[154:155], v[150:151]
	v_pk_mul_f32 v[152:153], v[4:5], v[178:179] op_sel_hi:[1,0]
	v_pk_mul_f32 v[154:155], v[6:7], v[178:179] op_sel_hi:[1,0]
	s_nop 0
	v_pk_fma_f32 v[154:155], v[130:131], v[154:155], v[146:147]
	v_pk_fma_f32 v[146:147], v[128:129], v[152:153], v[144:145]
	v_cvt_pk_bf16_f32 v144, v148, v149
	v_cvt_pk_bf16_f32 v145, v150, v151
	s_nop 0
	v_cvt_pk_bf16_f32 v146, v146, v147
	v_cvt_pk_bf16_f32 v147, v154, v155
	global_store_dwordx4 v[180:181], v[144:147], off offset:16
	v_add_u32_e32 v226, 0x80, v172
	v_ashrrev_i32_e32 v227, 31, v226
	v_lshlrev_b64 v[144:145], 13, v[226:227]
	v_add_u32_e32 v228, 0x90, v172
	v_lshl_add_u64 v[144:145], v[170:171], 0, v[144:145]
	v_ashrrev_i32_e32 v229, 31, v228
	global_load_dwordx4 v[152:155], v[144:145], off offset:48
	global_load_dwordx4 v[178:181], v[144:145], off offset:32
	global_load_dwordx4 v[182:185], v[144:145], off offset:16
	global_load_dwordx4 v[186:189], v[144:145], off
	v_lshlrev_b64 v[144:145], 13, v[228:229]
	v_add_u32_e32 v230, 0xa0, v172
	v_lshl_add_u64 v[144:145], v[170:171], 0, v[144:145]
	v_ashrrev_i32_e32 v231, 31, v230
	global_load_dwordx4 v[190:193], v[144:145], off offset:48
	global_load_dwordx4 v[194:197], v[144:145], off offset:32
	global_load_dwordx4 v[198:201], v[144:145], off offset:16
	global_load_dwordx4 v[202:205], v[144:145], off
	v_lshlrev_b64 v[144:145], 13, v[230:231]
	v_add_u32_e32 v232, 0xb0, v172
	v_lshl_add_u64 v[144:145], v[170:171], 0, v[144:145]
	v_ashrrev_i32_e32 v233, 31, v232
	global_load_dwordx4 v[206:209], v[144:145], off offset:48
	global_load_dwordx4 v[210:213], v[144:145], off offset:32
	global_load_dwordx4 v[214:217], v[144:145], off offset:16
	global_load_dwordx4 v[218:221], v[144:145], off
	v_lshlrev_b64 v[144:145], 13, v[232:233]
	v_lshl_add_u64 v[222:223], v[170:171], 0, v[144:145]
	global_load_dwordx4 v[144:147], v[222:223], off offset:48
	global_load_dwordx4 v[148:151], v[222:223], off offset:32
	global_load_dwordx4 v[170:173], v[222:223], off offset:16
	s_nop 0
	global_load_dwordx4 v[222:225], v[222:223], off
	ds_read_b32 v234, v159 offset:512
	v_lshlrev_b64 v[226:227], 12, v[226:227]
	v_lshl_add_u64 v[226:227], v[168:169], 0, v[226:227]
	s_waitcnt lgkmcnt(0)
	v_pk_mul_f32 v[236:237], v[80:81], v[234:235] op_sel_hi:[1,0]
	v_pk_mul_f32 v[238:239], v[82:83], v[234:235] op_sel_hi:[1,0]
	v_pk_mul_f32 v[240:241], v[72:73], v[234:235] op_sel_hi:[1,0]
	v_pk_mul_f32 v[242:243], v[74:75], v[234:235] op_sel_hi:[1,0]
	v_pk_mul_f32 v[244:245], v[16:17], v[234:235] op_sel_hi:[1,0]
	v_pk_mul_f32 v[246:247], v[18:19], v[234:235] op_sel_hi:[1,0]
	v_pk_mul_f32 v[248:249], v[0:1], v[234:235] op_sel_hi:[1,0]
	v_pk_mul_f32 v[234:235], v[2:3], v[234:235] op_sel_hi:[1,0]
	s_waitcnt vmcnt(14)
	v_pk_fma_f32 v[180:181], v[134:135], v[246:247], v[180:181]
	s_waitcnt vmcnt(13)
	v_pk_fma_f32 v[184:185], v[138:139], v[242:243], v[184:185]
	s_waitcnt vmcnt(12)
	v_pk_fma_f32 v[188:189], v[142:143], v[238:239], v[188:189]
	v_pk_fma_f32 v[186:187], v[140:141], v[236:237], v[186:187]
	v_pk_fma_f32 v[182:183], v[136:137], v[240:241], v[182:183]
	v_pk_fma_f32 v[178:179], v[132:133], v[244:245], v[178:179]
	v_pk_fma_f32 v[234:235], v[130:131], v[234:235], v[154:155]
	v_pk_fma_f32 v[236:237], v[128:129], v[248:249], v[152:153]
	v_cvt_pk_bf16_f32 v152, v186, v187
	v_cvt_pk_bf16_f32 v153, v188, v189
	v_cvt_pk_bf16_f32 v154, v182, v183
	v_cvt_pk_bf16_f32 v155, v184, v185
	v_cvt_pk_bf16_f32 v178, v178, v179
	v_cvt_pk_bf16_f32 v179, v180, v181
	s_nop 0
	v_cvt_pk_bf16_f32 v180, v236, v237
	v_cvt_pk_bf16_f32 v181, v234, v235
	global_store_dwordx4 v[226:227], v[152:155], off
	global_store_dwordx4 v[226:227], v[178:181], off offset:16
	ds_read_b32 v178, v159 offset:576
	v_lshlrev_b64 v[152:153], 12, v[228:229]
	v_lshl_add_u64 v[180:181], v[168:169], 0, v[152:153]
	s_waitcnt lgkmcnt(0)
	v_pk_mul_f32 v[152:153], v[64:65], v[178:179] op_sel_hi:[1,0]
	v_pk_mul_f32 v[154:155], v[66:67], v[178:179] op_sel_hi:[1,0]
	s_waitcnt vmcnt(10)
	v_pk_fma_f32 v[152:153], v[140:141], v[152:153], v[202:203]
	v_pk_fma_f32 v[154:155], v[142:143], v[154:155], v[204:205]
	v_pk_mul_f32 v[182:183], v[56:57], v[178:179] op_sel_hi:[1,0]
	v_pk_mul_f32 v[184:185], v[58:59], v[178:179] op_sel_hi:[1,0]
	v_pk_fma_f32 v[182:183], v[136:137], v[182:183], v[198:199]
	v_pk_fma_f32 v[184:185], v[138:139], v[184:185], v[200:201]
	v_cvt_pk_bf16_f32 v152, v152, v153
	v_cvt_pk_bf16_f32 v153, v154, v155
	v_cvt_pk_bf16_f32 v154, v182, v183
	v_pk_mul_f32 v[182:183], v[108:109], v[178:179] op_sel_hi:[1,0]
	v_cvt_pk_bf16_f32 v155, v184, v185
	global_store_dwordx4 v[180:181], v[152:155], off
	v_pk_fma_f32 v[182:183], v[128:129], v[182:183], v[190:191]
	s_nop 0
	v_pk_mul_f32 v[152:153], v[104:105], v[178:179] op_sel_hi:[1,0]
	v_pk_mul_f32 v[154:155], v[106:107], v[178:179] op_sel_hi:[1,0]
	v_pk_fma_f32 v[152:153], v[132:133], v[152:153], v[194:195]
	v_pk_fma_f32 v[154:155], v[134:135], v[154:155], v[196:197]
	v_pk_mul_f32 v[178:179], v[110:111], v[178:179] op_sel_hi:[1,0]
	v_cvt_pk_bf16_f32 v152, v152, v153
	v_cvt_pk_bf16_f32 v153, v154, v155
	v_cvt_pk_bf16_f32 v154, v182, v183
	s_nop 0
	v_pk_fma_f32 v[178:179], v[130:131], v[178:179], v[192:193]
	s_nop 0
	v_cvt_pk_bf16_f32 v155, v178, v179
	global_store_dwordx4 v[180:181], v[152:155], off offset:16
	ds_read_b32 v178, v159 offset:640
	s_nop 0
	v_lshlrev_b64 v[152:153], 12, v[230:231]
	v_lshl_add_u64 v[180:181], v[168:169], 0, v[152:153]
	s_waitcnt lgkmcnt(0)
	v_pk_mul_f32 v[152:153], v[48:49], v[178:179] op_sel_hi:[1,0]
	v_pk_mul_f32 v[154:155], v[50:51], v[178:179] op_sel_hi:[1,0]
	s_waitcnt vmcnt(8)
	v_pk_fma_f32 v[152:153], v[140:141], v[152:153], v[218:219]
	v_pk_fma_f32 v[154:155], v[142:143], v[154:155], v[220:221]
	v_pk_mul_f32 v[182:183], v[40:41], v[178:179] op_sel_hi:[1,0]
	v_pk_mul_f32 v[184:185], v[42:43], v[178:179] op_sel_hi:[1,0]
	v_pk_fma_f32 v[182:183], v[136:137], v[182:183], v[214:215]
	v_pk_fma_f32 v[184:185], v[138:139], v[184:185], v[216:217]
	v_cvt_pk_bf16_f32 v152, v152, v153
	v_cvt_pk_bf16_f32 v153, v154, v155
	v_cvt_pk_bf16_f32 v154, v182, v183
	v_pk_mul_f32 v[182:183], v[116:117], v[178:179] op_sel_hi:[1,0]
	v_cvt_pk_bf16_f32 v155, v184, v185
	global_store_dwordx4 v[180:181], v[152:155], off
	v_pk_fma_f32 v[182:183], v[128:129], v[182:183], v[206:207]
	s_nop 0
	v_pk_mul_f32 v[152:153], v[112:113], v[178:179] op_sel_hi:[1,0]
	v_pk_mul_f32 v[154:155], v[114:115], v[178:179] op_sel_hi:[1,0]
	v_pk_fma_f32 v[152:153], v[132:133], v[152:153], v[210:211]
	v_pk_fma_f32 v[154:155], v[134:135], v[154:155], v[212:213]
	v_pk_mul_f32 v[178:179], v[118:119], v[178:179] op_sel_hi:[1,0]
	v_cvt_pk_bf16_f32 v152, v152, v153
	v_cvt_pk_bf16_f32 v153, v154, v155
	v_cvt_pk_bf16_f32 v154, v182, v183
	s_nop 0
	v_pk_fma_f32 v[178:179], v[130:131], v[178:179], v[208:209]
	s_nop 0
	v_cvt_pk_bf16_f32 v155, v178, v179
	global_store_dwordx4 v[180:181], v[152:155], off offset:16
	ds_read_b32 v152, v159 offset:704
	s_nop 0
	v_lshlrev_b64 v[154:155], 12, v[232:233]
	v_lshl_add_u64 v[154:155], v[168:169], 0, v[154:155]
	s_waitcnt lgkmcnt(0)
	v_pk_mul_f32 v[168:169], v[32:33], v[152:153] op_sel_hi:[1,0]
	v_pk_mul_f32 v[178:179], v[34:35], v[152:153] op_sel_hi:[1,0]
	s_waitcnt vmcnt(6)
	v_pk_fma_f32 v[140:141], v[140:141], v[168:169], v[222:223]
	v_pk_fma_f32 v[142:143], v[142:143], v[178:179], v[224:225]
	v_pk_mul_f32 v[168:169], v[24:25], v[152:153] op_sel_hi:[1,0]
	v_pk_mul_f32 v[178:179], v[26:27], v[152:153] op_sel_hi:[1,0]
	s_nop 0
	v_pk_fma_f32 v[172:173], v[138:139], v[178:179], v[172:173]
	v_pk_fma_f32 v[138:139], v[136:137], v[168:169], v[170:171]
	v_cvt_pk_bf16_f32 v136, v140, v141
	v_cvt_pk_bf16_f32 v137, v142, v143
	s_nop 0
	v_cvt_pk_bf16_f32 v138, v138, v139
	v_cvt_pk_bf16_f32 v139, v172, v173
	global_store_dwordx4 v[154:155], v[136:139], off
	s_nop 1
	v_pk_mul_f32 v[136:137], v[120:121], v[152:153] op_sel_hi:[1,0]
	v_pk_mul_f32 v[138:139], v[122:123], v[152:153] op_sel_hi:[1,0]
	v_pk_fma_f32 v[132:133], v[132:133], v[136:137], v[148:149]
	v_pk_fma_f32 v[134:135], v[134:135], v[138:139], v[150:151]
	v_pk_mul_f32 v[136:137], v[124:125], v[152:153] op_sel_hi:[1,0]
	v_pk_mul_f32 v[138:139], v[126:127], v[152:153] op_sel_hi:[1,0]
	s_nop 0
	v_pk_fma_f32 v[138:139], v[130:131], v[138:139], v[146:147]
	v_pk_fma_f32 v[130:131], v[128:129], v[136:137], v[144:145]
	v_cvt_pk_bf16_f32 v128, v132, v133
	v_cvt_pk_bf16_f32 v129, v134, v135
	s_nop 0
	v_cvt_pk_bf16_f32 v130, v130, v131
	v_cvt_pk_bf16_f32 v131, v138, v139
	global_store_dwordx4 v[154:155], v[128:131], off offset:16
	s_and_b64 vcc, exec, s[2:3]
	v_readlane_b32 s61, v254, 15
	s_cbranch_vccnz .LBB0_647
	s_andn2_b64 vcc, exec, s[14:15]
	s_cbranch_vccnz .LBB0_624
	s_barrier
	s_branch .LBB0_624

.LBB0_896:
	v_readlane_b32 s3, v254, 10
	s_lshl_b32 s59, s2, 6
	v_ashrrev_i32_e32 v4, 5, v2
	s_lshl_b32 s2, s2, 13
	v_lshlrev_b32_e32 v1, 1, v2
	v_lshl_add_u32 v5, v4, 10, s2
	s_lshl_b32 s2, s3, 5
	v_and_b32_e32 v3, 32, v1
	v_lshlrev_b32_e32 v2, 6, v2
	s_and_b32 s60, s2, 0x60
	v_or_b32_e32 v6, v5, v3
	v_and_b32_e32 v2, 0x3c0, v2
	v_and_b32_e32 v1, 16, v1
	s_lshr_b32 s2, s60, 3
	v_or3_b32 v6, v6, v2, v1
	v_add_lshl_u32 v4, v4, s2, 10
	v_or_b32_e32 v2, v2, v3
	v_or3_b32 v194, v2, v4, v1
	v_or_b32_e32 v2, 16, v2
	v_mov_b32_e32 v177, 0
	v_bitop3_b32 v5, v2, v5, v1 bitop3:0xde
	v_bitop3_b32 v195, v2, v4, v1 bitop3:0xde
	s_waitcnt vmcnt(2)
	s_barrier
	s_mov_b64 s[14:15], 0x80
	v_lshl_add_u64 v[2:3], s[36:37], 0, v[176:177]
	s_add_i32 m0, s50, 0x18000
	v_lshl_add_u64 v[2:3], v[2:3], 0, s[14:15]
	s_add_i32 s58, s3, s49
	global_load_lds_dwordx4 v[2:3], off
	v_mov_b32_e32 v179, v177
	s_add_i32 m0, s50, 0x1a000
	s_add_u32 s2, s10, 0x36000080
	v_lshl_add_u64 v[2:3], s[36:37], 0, v[178:179]
	v_lshl_add_u64 v[2:3], v[2:3], 0, s[14:15]
	s_addc_u32 s3, s11, 0
	s_add_i32 s62, s50, 0x8000
	global_load_lds_dwordx4 v[2:3], off
	s_mov_b32 m0, s62
	s_add_i32 s63, s50, 0xa000
	s_mov_b64 s[16:17], 0x36000080
	global_load_lds_dwordx4 v180, s[2:3]
	s_mov_b32 m0, s63
	s_mov_b32 s61, 0x8000
	global_load_lds_dwordx4 v182, s[2:3]
	s_add_u32 s2, s36, 0x4080
	s_addc_u32 s3, s37, 0
	s_add_i32 m0, s50, 0x1c000
	s_movk_i32 s64, 0x100
	global_load_lds_dwordx4 v176, s[2:3]
	s_add_i32 m0, s50, 0x1e000
	v_mov_b32_e32 v184, v176
	global_load_lds_dwordx4 v178, s[2:3]
	s_waitcnt vmcnt(6)
	v_readlane_b32 s2, v254, 15
	s_cmpk_lt_u32 s2, 0x100
	s_cselect_b64 s[18:19], -1, 0
	s_add_i32 s65, s45, -1
	v_mov_b32_e32 v231, 0x24854
	v_mov_b32_e32 v252, 0x24858
	v_mov_b32_e32 v253, 0x2485c
	v_mov_b32_e32 v220, 0x24864
	v_mov_b32_e32 v221, 0x24868
	v_mov_b32_e32 v222, 0x2486c
	v_mov_b32_e32 v223, 0x24870
	v_mov_b32_e32 v224, 0x24874
	v_mov_b32_e32 v225, 0x24878
	v_mov_b32_e32 v226, 0x2487c
	s_mov_b32 s66, 0x25800
	s_add_i32 s67, 0, 0x10000
	s_add_i32 s68, 0, 0x14000
	v_add_u32_e32 v227, 0, v6
	v_add_u32_e32 v228, 0, v5
	v_mov_b32_e32 v229, 0x7f7f7f7f
	s_mov_b64 s[20:21], 0x5e000000
	s_mov_b32 s69, 0xc0c00000
	s_mov_b64 s[22:23], 0x22000000
	s_mov_b32 s70, 0x22001000
	v_mov_b32_e32 v230, 0x41000000
	v_mov_b32_e32 v176, v0
	s_mov_b32 s74, 0
	v_mov_b32_e32 v0, v177
	v_mov_b32_e32 v1, v177
	v_mov_b32_e32 v2, v177
	v_mov_b32_e32 v3, v177
	v_mov_b32_e32 v4, v177
	v_mov_b32_e32 v5, v177
	v_mov_b32_e32 v6, v177
	v_mov_b32_e32 v7, v177
	v_mov_b32_e32 v8, v177
	v_mov_b32_e32 v9, v177
	v_mov_b32_e32 v10, v177
	v_mov_b32_e32 v11, v177
	v_mov_b32_e32 v12, v177
	v_mov_b32_e32 v13, v177
	v_mov_b32_e32 v14, v177
	v_mov_b32_e32 v15, v177
	v_mov_b32_e32 v16, v177
	v_mov_b32_e32 v17, v177
	v_mov_b32_e32 v18, v177
	v_mov_b32_e32 v19, v177
	v_mov_b32_e32 v20, v177
	v_mov_b32_e32 v21, v177
	v_mov_b32_e32 v22, v177
	v_mov_b32_e32 v23, v177
	v_mov_b32_e32 v24, v177
	v_mov_b32_e32 v25, v177
	v_mov_b32_e32 v26, v177
	v_mov_b32_e32 v27, v177
	v_mov_b32_e32 v28, v177
	v_mov_b32_e32 v29, v177
	v_mov_b32_e32 v30, v177
	v_mov_b32_e32 v31, v177
	v_mov_b32_e32 v36, v177
	v_mov_b32_e32 v37, v177
	v_mov_b32_e32 v38, v177
	v_mov_b32_e32 v39, v177
	v_mov_b32_e32 v44, v177
	v_mov_b32_e32 v45, v177
	v_mov_b32_e32 v46, v177
	v_mov_b32_e32 v47, v177
	v_mov_b32_e32 v32, v177
	v_mov_b32_e32 v33, v177
	v_mov_b32_e32 v34, v177
	v_mov_b32_e32 v35, v177
	v_mov_b32_e32 v40, v177
	v_mov_b32_e32 v41, v177
	v_mov_b32_e32 v42, v177
	v_mov_b32_e32 v43, v177
	v_mov_b32_e32 v48, v177
	v_mov_b32_e32 v49, v177
	v_mov_b32_e32 v50, v177
	v_mov_b32_e32 v51, v177
	v_mov_b32_e32 v52, v177
	v_mov_b32_e32 v53, v177
	v_mov_b32_e32 v54, v177
	v_mov_b32_e32 v55, v177
	v_mov_b32_e32 v56, v177
	v_mov_b32_e32 v57, v177
	v_mov_b32_e32 v58, v177
	v_mov_b32_e32 v59, v177
	v_mov_b32_e32 v60, v177
	v_mov_b32_e32 v61, v177
	v_mov_b32_e32 v62, v177
	v_mov_b32_e32 v63, v177
	v_mov_b32_e32 v64, v177
	v_mov_b32_e32 v65, v177
	v_mov_b32_e32 v66, v177
	v_mov_b32_e32 v67, v177
	v_mov_b32_e32 v68, v177
	v_mov_b32_e32 v69, v177
	v_mov_b32_e32 v70, v177
	v_mov_b32_e32 v71, v177
	v_mov_b32_e32 v72, v177
	v_mov_b32_e32 v73, v177
	v_mov_b32_e32 v74, v177
	v_mov_b32_e32 v75, v177
	v_mov_b32_e32 v76, v177
	v_mov_b32_e32 v77, v177
	v_mov_b32_e32 v78, v177
	v_mov_b32_e32 v79, v177
	v_mov_b32_e32 v80, v177
	v_mov_b32_e32 v81, v177
	v_mov_b32_e32 v82, v177
	v_mov_b32_e32 v83, v177
	v_mov_b32_e32 v84, v177
	v_mov_b32_e32 v85, v177
	v_mov_b32_e32 v86, v177
	v_mov_b32_e32 v87, v177
	v_mov_b32_e32 v88, v177
	v_mov_b32_e32 v89, v177
	v_mov_b32_e32 v90, v177
	v_mov_b32_e32 v91, v177
	v_mov_b32_e32 v92, v177
	v_mov_b32_e32 v93, v177
	v_mov_b32_e32 v94, v177
	v_mov_b32_e32 v95, v177
	v_mov_b32_e32 v96, v177
	v_mov_b32_e32 v97, v177
	v_mov_b32_e32 v98, v177
	v_mov_b32_e32 v99, v177
	v_mov_b32_e32 v100, v177
	v_mov_b32_e32 v101, v177
	v_mov_b32_e32 v102, v177
	v_mov_b32_e32 v103, v177
	v_mov_b32_e32 v104, v177
	v_mov_b32_e32 v105, v177
	v_mov_b32_e32 v106, v177
	v_mov_b32_e32 v107, v177
	v_mov_b32_e32 v108, v177
	v_mov_b32_e32 v109, v177
	v_mov_b32_e32 v110, v177
	v_mov_b32_e32 v111, v177
	v_mov_b32_e32 v112, v177
	v_mov_b32_e32 v113, v177
	v_mov_b32_e32 v114, v177
	v_mov_b32_e32 v115, v177
	v_mov_b32_e32 v116, v177
	v_mov_b32_e32 v117, v177
	v_mov_b32_e32 v118, v177
	v_mov_b32_e32 v119, v177
	v_mov_b32_e32 v120, v177
	v_mov_b32_e32 v121, v177
	v_mov_b32_e32 v122, v177
	v_mov_b32_e32 v123, v177
	v_mov_b32_e32 v124, v177
	v_mov_b32_e32 v125, v177
	v_mov_b32_e32 v126, v177
	v_mov_b32_e32 v127, v177
	s_barrier
.LBB0_897:
	v_readlane_b32 s2, v254, 13
	v_readlane_b32 s3, v254, 14
	s_mov_b32 s2, s99
	s_add_i32 s73, s74, 1
	v_readlane_b32 s3, v254, 11
	s_waitcnt lgkmcnt(0)
	s_mul_i32 s2, s73, s2
	s_add_i32 s2, s2, s3
	s_cmp_lt_i32 s2, s47
	s_cselect_b64 s[34:35], -1, 0
	s_cmp_ge_i32 s2, s47
	s_cselect_b64 s[28:29], -1, 0
	s_and_b64 vcc, exec, s[28:29]
	s_cbranch_vccnz .LBB0_899
	s_and_b32 s3, s2, 7
	s_lshr_b32 s7, s2, 3
	s_lshl_b32 s25, s46, 1
	s_mul_i32 s3, s3, s25
	s_add_i32 s2, s3, s7
	s_lshr_b32 s3, s2, 7
	s_lshl_b32 s7, s3, 3
	s_and_b32 s2, s2, 127
	s_sub_i32 s25, s46, s7
	s_min_i32 s25, s25, 8
	v_mbcnt_lo_u32_b32 v128, -1, 0
	v_mbcnt_hi_u32_b32 v128, -1, v128
	v_lshlrev_b32_e32 v128, 2, v128
	v_add_u32_e32 v128, 0x24800, v128
	ds_read_b32 v129, v128
	s_cmp_eq_u32 s25, 8
	s_cbranch_scc0 .Lsched_slow_p6
	s_lshr_b32 s24, s2, 3
	s_and_b32 s2, s2, 7
	s_branch .Lsched_done_p6

.LBB0_899:
	v_cndmask_b32_e64 v128, 0, 1, s[34:35]
	v_cmp_ne_u32_e64 s[2:3], 1, v128
	s_andn2_b64 vcc, exec, s[34:35]
	s_mov_b64 s[30:31], s[36:37]
	s_cbranch_vccnz .LBB0_901
	v_readlane_b32 s30, v254, 13
	v_readlane_b32 s31, v254, 14
	s_mov_b64 s[30:31], s[100:101]
	s_ashr_i32 s27, s26, 31
	s_lshl_b64 s[38:39], s[26:27], 23
	s_waitcnt lgkmcnt(0)
	s_add_u32 s7, s30, s38
	s_addc_u32 s27, s31, s39
	s_ashr_i32 s25, s24, 31
	s_lshl_b64 s[30:31], s[24:25], 19
	s_add_u32 s7, s7, s30
	s_addc_u32 s25, s27, s31
	s_add_u32 s30, s7, 0x2000000
	s_addc_u32 s31, s25, 0

.LBB0_904:
	s_cmp_lg_u32 s48, s71
	s_cselect_b64 s[38:39], -1, 0
	s_and_b64 s[38:39], s[34:35], s[38:39]
	s_andn2_b64 vcc, exec, s[38:39]
	s_cbranch_vccnz .LBB0_910
	v_mbcnt_lo_u32_b32 v128, -1, 0
	v_mbcnt_hi_u32_b32 v128, -1, v128
	s_xor_b32 s55, s55, 1
	v_add_u32_e32 v130, s33, v128
	v_cmp_gt_i32_e32 vcc, s64, v130
	s_and_saveexec_b64 s[38:39], vcc
	s_cbranch_execz .LBB0_909
	s_lshl_b32 s7, s26, 2
	v_readlane_b32 s42, v254, 13
	s_add_i32 s7, s7, 0x248a0
	v_readlane_b32 s43, v254, 14
	v_mov_b32_e32 v128, s7
	ds_read_b32 v129, v128
	v_lshl_add_u32 v128, s72, 8, v130
	s_waitcnt lgkmcnt(0)
	v_cmp_lt_i32_e32 vcc, v128, v129
	v_mov_b32_e32 v129, 0
	s_and_saveexec_b64 s[40:41], vcc
	s_cbranch_execz .LBB0_908
	s_mov_b64 s[42:43], s[100:101]
	s_ashr_i32 s27, s26, 31
	s_lshl_b64 s[76:77], s[26:27], 17
	v_ashrrev_i32_e32 v129, 31, v128
	s_waitcnt lgkmcnt(0)
	s_add_u32 s42, s42, s76
	s_addc_u32 s43, s43, s77
	v_lshl_add_u64 v[128:129], v[128:129], 2, s[42:43]
	v_add_co_u32_e32 v128, vcc, 0x1a00000, v128
	s_nop 1
	v_addc_co_u32_e32 v129, vcc, 0, v129, vcc
	global_load_dword v128, v[128:129], off
	s_waitcnt vmcnt(0)
	v_lshlrev_b32_e32 v128, 9, v128
	v_and_b32_e32 v129, 0xfffff800, v128

.LBB0_910:
	s_add_u32 s25, s36, 0x100
	s_addc_u32 s27, s37, 0
	s_lshl_b32 s7, s55, 10
	s_add_i32 s7, s7, 0x24000
	s_mov_b32 s42, -2
	s_mov_b64 s[36:37], 0
	s_cmp_eq_u32 s42, 12
	s_cselect_b64 s[40:41], -1, 0
	s_and_b64 s[38:39], s[34:35], s[40:41]
	s_andn2_b64 vcc, exec, s[38:39]
	v_mov_b32_e32 v128, v186
	v_mov_b32_e32 v129, v176
	s_add_u32 s76, s10, s36
	v_add_u32_e32 v134, s67, v194
	v_add_u32_e32 v142, s67, v195
	v_add_u32_e32 v150, s68, v194
	v_add_u32_e32 v158, s68, v195
	s_addc_u32 s77, s11, s37
	ds_read_b128 v[130:133], v134
	ds_read_b128 v[138:141], v134 offset:2048
	ds_read_b128 v[134:137], v142
	ds_read_b128 v[142:145], v142 offset:2048
	ds_read_b128 v[146:149], v150
	ds_read_b128 v[154:157], v150 offset:2048
	ds_read_b128 v[150:153], v158
	ds_read_b128 v[158:161], v158 offset:2048
	s_add_u32 s43, s76, 0x36000100
	s_addc_u32 s75, s77, 0
	s_and_b64 s[38:39], s[40:41], exec
	s_cselect_b32 s39, s13, s75
	s_cselect_b32 s38, s12, s43
	s_add_u32 s43, s25, s36
	s_addc_u32 s75, s27, s37
	s_and_b64 s[40:41], s[40:41], exec
	s_cselect_b32 s41, s31, s75
	s_cselect_b32 s40, s30, s43
	ds_read_b128 v[162:165], v227
	ds_read_b128 v[232:235], v227 offset:2048
	ds_read_b128 v[166:169], v228
	ds_read_b128 v[236:239], v228 offset:2048
	ds_read_b128 v[240:243], v227 offset:4096
	ds_read_b128 v[196:199], v227 offset:6144
	ds_read_b128 v[244:247], v228 offset:4096
	ds_read_b128 v[200:203], v228 offset:6144
	s_add_i32 m0, s50, 0xc000
	v_lshl_add_u64 v[170:171], s[76:77], 0, v[176:177]
	v_lshl_add_u64 v[170:171], v[170:171], 0, s[16:17]
	v_mov_b32_e32 v187, v177
	global_load_lds_dwordx4 v[170:171], off
	s_add_i32 m0, s50, 0xe000
	v_lshl_add_u64 v[170:171], s[76:77], 0, v[186:187]
	v_lshl_add_u64 v[170:171], v[170:171], 0, s[16:17]
	global_load_lds_dwordx4 v[170:171], off
	s_waitcnt vmcnt(8)
	s_waitcnt lgkmcnt(0)
	s_barrier
	s_setprio 1
	s_waitcnt lgkmcnt(0)
	v_mfma_scale_f32_16x16x128_f8f6f4 v[100:103], v[130:137], v[162:169], 0, v229, v229 op_sel_hi:[0,0,0]
	v_mfma_scale_f32_16x16x128_f8f6f4 v[96:99], v[138:145], v[162:169], 0, v229, v229 op_sel_hi:[0,0,0]
	v_mfma_scale_f32_16x16x128_f8f6f4 v[92:95], v[130:137], v[232:239], 0, v229, v229 op_sel_hi:[0,0,0]
	v_mfma_scale_f32_16x16x128_f8f6f4 v[88:91], v[138:145], v[232:239], 0, v229, v229 op_sel_hi:[0,0,0]
	v_mfma_scale_f32_16x16x128_f8f6f4 v[84:87], v[130:137], v[240:247], 0, v229, v229 op_sel_hi:[0,0,0]
	v_mfma_scale_f32_16x16x128_f8f6f4 v[80:83], v[138:145], v[240:247], 0, v229, v229 op_sel_hi:[0,0,0]
	v_mfma_scale_f32_16x16x128_f8f6f4 v[170:173], v[130:137], v[196:203], 0, v229, v229 op_sel_hi:[0,0,0]
	v_mfma_scale_f32_16x16x128_f8f6f4 v[188:191], v[138:145], v[196:203], 0, v229, v229 op_sel_hi:[0,0,0]
	s_setprio 0
	s_setprio 1
	v_mfma_scale_f32_16x16x128_f8f6f4 v[40:43], v[146:153], v[196:203], 0, v229, v229 op_sel_hi:[0,0,0]
	v_mfma_scale_f32_16x16x128_f8f6f4 v[32:35], v[154:161], v[196:203], 0, v229, v229 op_sel_hi:[0,0,0]
	v_mfma_scale_f32_16x16x128_f8f6f4 v[248:251], v[146:153], v[162:169], 0, v229, v229 op_sel_hi:[0,0,0]
	v_mfma_scale_f32_16x16x128_f8f6f4 v[204:207], v[154:161], v[162:169], 0, v229, v229 op_sel_hi:[0,0,0]
	v_mfma_scale_f32_16x16x128_f8f6f4 v[208:211], v[146:153], v[232:239], 0, v229, v229 op_sel_hi:[0,0,0]
	v_mfma_scale_f32_16x16x128_f8f6f4 v[212:215], v[154:161], v[232:239], 0, v229, v229 op_sel_hi:[0,0,0]
	v_mfma_scale_f32_16x16x128_f8f6f4 v[216:219], v[146:153], v[240:247], 0, v229, v229 op_sel_hi:[0,0,0]
	v_mfma_scale_f32_16x16x128_f8f6f4 v[240:243], v[154:161], v[240:247], 0, v229, v229 op_sel_hi:[0,0,0]
	s_setprio 0
	s_barrier
	s_add_i32 s43, s67, s5
	s_mov_b32 m0, s43
	s_nop 2
	ds_read_b128 v[48:51], v227 offset:16384
	ds_read_b128 v[56:59], v227 offset:18432
	ds_read_b128 v[52:55], v228 offset:16384
	ds_read_b128 v[60:63], v228 offset:18432
	ds_read_b128 v[64:67], v227 offset:20480
	ds_read_b128 v[72:75], v227 offset:22528
	ds_read_b128 v[68:71], v228 offset:20480
	ds_read_b128 v[76:79], v228 offset:22528
	s_nop 0
	global_load_lds_dwordx4 v184, s[40:41]
	s_add_i32 m0, s43, 0x2000
	s_add_u32 s76, s40, 0x4000
	s_addc_u32 s77, s41, 0
	s_add_i32 s43, s68, s5
	s_nop 0
	global_load_lds_dwordx4 v178, s[40:41]
	s_mov_b32 m0, s43
	s_nop 0
	global_load_lds_dwordx4 v184, s[76:77]
	s_add_i32 m0, s43, 0x2000
	s_nop 0
	global_load_lds_dwordx4 v178, s[76:77]
	s_mov_b32 m0, s50
	s_nop 0
	global_load_lds_dwordx4 v180, s[38:39]
	s_mov_b32 m0, s51
	s_nop 0
	global_load_lds_dwordx4 v182, s[38:39]
	s_waitcnt vmcnt(8)
	s_waitcnt lgkmcnt(0)
	s_barrier
	s_setprio 1
	s_waitcnt lgkmcnt(0)
	v_mfma_scale_f32_16x16x128_f8f6f4 v[44:47], v[130:137], v[48:55], 0, v229, v229 op_sel_hi:[0,0,0]
	v_mfma_scale_f32_16x16x128_f8f6f4 v[36:39], v[138:145], v[48:55], 0, v229, v229 op_sel_hi:[0,0,0]
	v_mfma_scale_f32_16x16x128_f8f6f4 v[28:31], v[130:137], v[56:63], 0, v229, v229 op_sel_hi:[0,0,0]
	v_mfma_scale_f32_16x16x128_f8f6f4 v[24:27], v[138:145], v[56:63], 0, v229, v229 op_sel_hi:[0,0,0]
	v_mfma_scale_f32_16x16x128_f8f6f4 v[20:23], v[130:137], v[64:71], 0, v229, v229 op_sel_hi:[0,0,0]
	v_mfma_scale_f32_16x16x128_f8f6f4 v[16:19], v[138:145], v[64:71], 0, v229, v229 op_sel_hi:[0,0,0]
	v_mfma_scale_f32_16x16x128_f8f6f4 v[12:15], v[130:137], v[72:79], 0, v229, v229 op_sel_hi:[0,0,0]
	v_mfma_scale_f32_16x16x128_f8f6f4 v[8:11], v[138:145], v[72:79], 0, v229, v229 op_sel_hi:[0,0,0]
	s_setprio 0
	s_setprio 1
	v_mfma_scale_f32_16x16x128_f8f6f4 v[4:7], v[146:153], v[48:55], 0, v229, v229 op_sel_hi:[0,0,0]
	v_mfma_scale_f32_16x16x128_f8f6f4 v[0:3], v[154:161], v[48:55], 0, v229, v229 op_sel_hi:[0,0,0]
	v_mfma_scale_f32_16x16x128_f8f6f4 v[104:107], v[146:153], v[56:63], 0, v229, v229 op_sel_hi:[0,0,0]
	v_mfma_scale_f32_16x16x128_f8f6f4 v[108:111], v[154:161], v[56:63], 0, v229, v229 op_sel_hi:[0,0,0]
	v_mfma_scale_f32_16x16x128_f8f6f4 v[112:115], v[146:153], v[64:71], 0, v229, v229 op_sel_hi:[0,0,0]
	v_mfma_scale_f32_16x16x128_f8f6f4 v[116:119], v[154:161], v[64:71], 0, v229, v229 op_sel_hi:[0,0,0]
	v_mfma_scale_f32_16x16x128_f8f6f4 v[120:123], v[146:153], v[72:79], 0, v229, v229 op_sel_hi:[0,0,0]
	v_mfma_scale_f32_16x16x128_f8f6f4 v[124:127], v[154:161], v[72:79], 0, v229, v229 op_sel_hi:[0,0,0]
	s_setprio 0
	s_barrier
	s_add_i32 s43, 0, 0x18000
	v_add_u32_e32 v48, s43, v194
	s_add_i32 s75, 0, 0x1c000
	v_add_u32_e32 v49, s43, v195
	ds_read_b128 v[130:133], v48
	ds_read_b128 v[138:141], v48 offset:2048
	ds_read_b128 v[134:137], v49
	ds_read_b128 v[142:145], v49 offset:2048
	v_add_u32_e32 v48, s75, v194
	v_add_u32_e32 v49, s75, v195
	ds_read_b128 v[146:149], v48
	ds_read_b128 v[154:157], v48 offset:2048
	ds_read_b128 v[150:153], v49
	ds_read_b128 v[158:161], v49 offset:2048
	s_mov_b32 m0, s52
	v_mov_b32_e32 v176, v129
	ds_read_b128 v[48:51], v227 offset:32768
	ds_read_b128 v[162:165], v227 offset:34816
	ds_read_b128 v[52:55], v228 offset:32768
	ds_read_b128 v[166:169], v228 offset:34816
	ds_read_b128 v[196:199], v227 offset:36864
	ds_read_b128 v[232:235], v227 offset:38912
	ds_read_b128 v[200:203], v228 offset:36864
	ds_read_b128 v[236:239], v228 offset:38912
	v_mov_b32_e32 v186, v128
	global_load_lds_dwordx4 v176, s[38:39]
	s_mov_b32 m0, s53
	s_nop 0
	global_load_lds_dwordx4 v186, s[38:39]
	s_waitcnt vmcnt(8)
	s_waitcnt lgkmcnt(0)
	s_barrier
	s_setprio 1
	s_waitcnt lgkmcnt(0)
	v_mfma_scale_f32_16x16x128_f8f6f4 v[100:103], v[130:137], v[48:55], v[100:103], v229, v229 op_sel_hi:[0,0,0]
	v_mfma_scale_f32_16x16x128_f8f6f4 v[96:99], v[138:145], v[48:55], v[96:99], v229, v229 op_sel_hi:[0,0,0]
	v_mfma_scale_f32_16x16x128_f8f6f4 v[92:95], v[130:137], v[162:169], v[92:95], v229, v229 op_sel_hi:[0,0,0]
	v_mfma_scale_f32_16x16x128_f8f6f4 v[88:91], v[138:145], v[162:169], v[88:91], v229, v229 op_sel_hi:[0,0,0]
	v_mfma_scale_f32_16x16x128_f8f6f4 v[84:87], v[130:137], v[196:203], v[84:87], v229, v229 op_sel_hi:[0,0,0]
	v_mfma_scale_f32_16x16x128_f8f6f4 v[80:83], v[138:145], v[196:203], v[80:83], v229, v229 op_sel_hi:[0,0,0]
	v_mfma_scale_f32_16x16x128_f8f6f4 v[76:79], v[130:137], v[232:239], v[170:173], v229, v229 op_sel_hi:[0,0,0]
	v_mfma_scale_f32_16x16x128_f8f6f4 v[72:75], v[138:145], v[232:239], v[188:191], v229, v229 op_sel_hi:[0,0,0]
	s_setprio 0
	s_setprio 1
	v_mfma_scale_f32_16x16x128_f8f6f4 v[68:71], v[146:153], v[48:55], v[248:251], v229, v229 op_sel_hi:[0,0,0]
	v_mfma_scale_f32_16x16x128_f8f6f4 v[64:67], v[154:161], v[48:55], v[204:207], v229, v229 op_sel_hi:[0,0,0]
	v_mfma_scale_f32_16x16x128_f8f6f4 v[60:63], v[146:153], v[162:169], v[208:211], v229, v229 op_sel_hi:[0,0,0]
	v_mfma_scale_f32_16x16x128_f8f6f4 v[56:59], v[154:161], v[162:169], v[212:215], v229, v229 op_sel_hi:[0,0,0]
	v_mfma_scale_f32_16x16x128_f8f6f4 v[52:55], v[146:153], v[196:203], v[216:219], v229, v229 op_sel_hi:[0,0,0]
	v_mfma_scale_f32_16x16x128_f8f6f4 v[48:51], v[154:161], v[196:203], v[240:243], v229, v229 op_sel_hi:[0,0,0]
	v_mfma_scale_f32_16x16x128_f8f6f4 v[40:43], v[146:153], v[232:239], v[40:43], v229, v229 op_sel_hi:[0,0,0]
	v_mfma_scale_f32_16x16x128_f8f6f4 v[32:35], v[154:161], v[232:239], v[32:35], v229, v229 op_sel_hi:[0,0,0]
	s_setprio 0
	s_barrier
	v_mov_b32_e32 v185, v177
	ds_read_b128 v[162:165], v227 offset:49152
	ds_read_b128 v[196:199], v227 offset:51200
	ds_read_b128 v[166:169], v228 offset:49152
	ds_read_b128 v[200:203], v228 offset:51200
	ds_read_b128 v[232:235], v227 offset:53248
	ds_read_b128 v[240:243], v227 offset:55296
	ds_read_b128 v[236:239], v228 offset:53248
	ds_read_b128 v[244:247], v228 offset:55296
	s_add_i32 s43, s43, s5
	v_lshl_add_u64 v[128:129], s[40:41], 0, v[184:185]
	v_lshl_add_u64 v[128:129], v[128:129], 0, s[14:15]
	s_mov_b32 m0, s43
	v_mov_b32_e32 v179, v177
	global_load_lds_dwordx4 v[128:129], off
	s_add_i32 m0, s43, 0x2000
	v_mov_b32_e32 v181, v177
	v_lshl_add_u64 v[128:129], s[40:41], 0, v[178:179]
	s_add_u32 s40, s40, 0x4080
	v_lshl_add_u64 v[128:129], v[128:129], 0, s[14:15]
	s_addc_u32 s41, s41, 0
	s_add_i32 s43, s75, s5
	global_load_lds_dwordx4 v[128:129], off
	s_mov_b32 m0, s43
	v_mov_b32_e32 v183, v177
	global_load_lds_dwordx4 v184, s[40:41]
	s_add_i32 m0, s43, 0x2000
	s_nop 0
	global_load_lds_dwordx4 v178, s[40:41]
	s_mov_b32 m0, s62
	v_lshl_add_u64 v[128:129], s[38:39], 0, v[180:181]
	v_lshl_add_u64 v[128:129], v[128:129], 0, s[14:15]
	global_load_lds_dwordx4 v[128:129], off
	s_mov_b32 m0, s63
	v_lshl_add_u64 v[128:129], s[38:39], 0, v[182:183]
	v_lshl_add_u64 v[128:129], v[128:129], 0, s[14:15]
	global_load_lds_dwordx4 v[128:129], off
	s_waitcnt vmcnt(8)
	s_waitcnt lgkmcnt(0)
	s_barrier
	s_setprio 1
	s_waitcnt lgkmcnt(0)
	v_mfma_scale_f32_16x16x128_f8f6f4 v[44:47], v[130:137], v[162:169], v[44:47], v229, v229 op_sel_hi:[0,0,0]
	v_mfma_scale_f32_16x16x128_f8f6f4 v[36:39], v[138:145], v[162:169], v[36:39], v229, v229 op_sel_hi:[0,0,0]
	v_mfma_scale_f32_16x16x128_f8f6f4 v[28:31], v[130:137], v[196:203], v[28:31], v229, v229 op_sel_hi:[0,0,0]
	v_mfma_scale_f32_16x16x128_f8f6f4 v[24:27], v[138:145], v[196:203], v[24:27], v229, v229 op_sel_hi:[0,0,0]
	v_mfma_scale_f32_16x16x128_f8f6f4 v[20:23], v[130:137], v[232:239], v[20:23], v229, v229 op_sel_hi:[0,0,0]
	v_mfma_scale_f32_16x16x128_f8f6f4 v[16:19], v[138:145], v[232:239], v[16:19], v229, v229 op_sel_hi:[0,0,0]
	v_mfma_scale_f32_16x16x128_f8f6f4 v[12:15], v[130:137], v[240:247], v[12:15], v229, v229 op_sel_hi:[0,0,0]
	v_mfma_scale_f32_16x16x128_f8f6f4 v[8:11], v[138:145], v[240:247], v[8:11], v229, v229 op_sel_hi:[0,0,0]
	s_setprio 0
	s_setprio 1
	v_mfma_scale_f32_16x16x128_f8f6f4 v[4:7], v[146:153], v[162:169], v[4:7], v229, v229 op_sel_hi:[0,0,0]
	v_mfma_scale_f32_16x16x128_f8f6f4 v[0:3], v[154:161], v[162:169], v[0:3], v229, v229 op_sel_hi:[0,0,0]
	v_mfma_scale_f32_16x16x128_f8f6f4 v[104:107], v[146:153], v[196:203], v[104:107], v229, v229 op_sel_hi:[0,0,0]
	v_mfma_scale_f32_16x16x128_f8f6f4 v[108:111], v[154:161], v[196:203], v[108:111], v229, v229 op_sel_hi:[0,0,0]
	v_mfma_scale_f32_16x16x128_f8f6f4 v[112:115], v[146:153], v[232:239], v[112:115], v229, v229 op_sel_hi:[0,0,0]
	v_mfma_scale_f32_16x16x128_f8f6f4 v[116:119], v[154:161], v[232:239], v[116:119], v229, v229 op_sel_hi:[0,0,0]
	v_mfma_scale_f32_16x16x128_f8f6f4 v[120:123], v[146:153], v[240:247], v[120:123], v229, v229 op_sel_hi:[0,0,0]
	v_mfma_scale_f32_16x16x128_f8f6f4 v[124:127], v[154:161], v[240:247], v[124:127], v229, v229 op_sel_hi:[0,0,0]
	s_setprio 0
	s_barrier
	s_add_i32 s42, s42, 2
	s_add_u32 s36, s36, 0x100
	s_addc_u32 s37, s37, 0
	s_branch .LBB0_912

.LBB0_916:
	s_add_u32 s34, s25, 0xffffff00
	s_addc_u32 s35, s27, -1
	v_readlane_b32 s42, v254, 13
	v_readlane_b32 s43, v254, 14
	v_mbcnt_lo_u32_b32 v183, -1, 0
	v_mbcnt_hi_u32_b32 v183, -1, v183
	s_bitcmp1_b32 s74, 0
	s_cselect_b32 s25, s66, 0x24c00
	s_lshl_b32 s27, s60, 2
	s_or_b32 s25, s25, s27
	v_and_b32_e32 v181, 15, v183
	v_ashrrev_i32_e32 v183, 1, v183
	v_and_b32_e32 v183, -8, v183
	v_lshl_add_u32 v179, v183, 2, s25
	ds_read_b128 v[172:175], v179
	ds_read_b128 v[160:163], v179 offset:16
	ds_read_b128 v[168:171], v179 offset:512
	ds_read_b128 v[164:167], v179 offset:528
	s_lshl_b32 s25, s48, 8
	s_add_i32 s25, s25, s59
	s_lshl_b32 s27, s4, 7
	s_or_b32 s27, s27, s60
	v_or_b32_e32 v181, s25, v181
	v_add_u32_e32 v183, s27, v183
	v_lshl_add_u32 v181, v181, 11, v183
	s_add_u32 s40, s100, s20
	s_addc_u32 s41, s101, s21
	v_mov_b32_e32 v200, 0x3b800000
	v_mov_b32_e32 v201, 0xc01d265f
	s_waitcnt lgkmcnt(0)
	v_pk_add_f32 v[168:169], v[168:169], 1.0 op_sel_hi:[1,0]
	v_pk_add_f32 v[170:171], v[170:171], 1.0 op_sel_hi:[1,0]
	v_pk_add_f32 v[164:165], v[164:165], 1.0 op_sel_hi:[1,0]
	v_pk_add_f32 v[166:167], v[166:167], 1.0 op_sel_hi:[1,0]
	v_pk_fma_f32 v[100:101], v[100:101], v[200:201], v[172:173] op_sel_hi:[1,0,1]
	v_pk_fma_f32 v[102:103], v[102:103], v[200:201], v[174:175] op_sel_hi:[1,0,1]
	v_pk_fma_f32 v[96:97], v[96:97], v[200:201], v[160:161] op_sel_hi:[1,0,1]
	v_pk_fma_f32 v[98:99], v[98:99], v[200:201], v[162:163] op_sel_hi:[1,0,1]
	v_min_f32_e32 v100, 0x40e00000, v100
	v_min_f32_e32 v101, 0x40e00000, v101
	v_min_f32_e32 v102, 0x40e00000, v102
	v_min_f32_e32 v103, 0x40e00000, v103
	v_min_f32_e32 v96, 0x40e00000, v96
	v_min_f32_e32 v97, 0x40e00000, v97
	v_min_f32_e32 v98, 0x40e00000, v98
	v_min_f32_e32 v99, 0x40e00000, v99
	v_pk_mul_f32 v[188:189], v[100:101], v[200:201] op_sel:[0,1] op_sel_hi:[1,1]
	v_pk_mul_f32 v[190:191], v[102:103], v[200:201] op_sel:[0,1] op_sel_hi:[1,1]
	v_pk_mul_f32 v[196:197], v[96:97], v[200:201] op_sel:[0,1] op_sel_hi:[1,1]
	v_pk_mul_f32 v[198:199], v[98:99], v[200:201] op_sel:[0,1] op_sel_hi:[1,1]
	v_exp_f32_e32 v188, v188
	v_exp_f32_e32 v189, v189
	v_exp_f32_e32 v190, v190
	v_exp_f32_e32 v191, v191
	v_exp_f32_e32 v196, v196
	v_exp_f32_e32 v197, v197
	v_exp_f32_e32 v198, v198
	v_exp_f32_e32 v199, v199
	v_pk_fma_f32 v[68:69], v[68:69], v[200:201], v[168:169] op_sel_hi:[1,0,1]
	v_pk_fma_f32 v[70:71], v[70:71], v[200:201], v[170:171] op_sel_hi:[1,0,1]
	v_pk_fma_f32 v[64:65], v[64:65], v[200:201], v[164:165] op_sel_hi:[1,0,1]
	v_pk_fma_f32 v[66:67], v[66:67], v[200:201], v[166:167] op_sel_hi:[1,0,1]
	v_pk_add_f32 v[188:189], v[188:189], 1.0 op_sel_hi:[1,0]
	v_pk_add_f32 v[190:191], v[190:191], 1.0 op_sel_hi:[1,0]
	v_pk_add_f32 v[196:197], v[196:197], 1.0 op_sel_hi:[1,0]
	v_pk_add_f32 v[198:199], v[198:199], 1.0 op_sel_hi:[1,0]
	v_rcp_f32_e32 v188, v188
	v_rcp_f32_e32 v189, v189
	v_rcp_f32_e32 v190, v190
	v_rcp_f32_e32 v191, v191
	v_rcp_f32_e32 v196, v196
	v_rcp_f32_e32 v197, v197
	v_rcp_f32_e32 v198, v198
	v_rcp_f32_e32 v199, v199
	v_med3_f32 v68, v68, s69, v230
	v_med3_f32 v69, v69, s69, v230
	v_med3_f32 v70, v70, s69, v230
	v_med3_f32 v71, v71, s69, v230
	v_med3_f32 v64, v64, s69, v230
	v_med3_f32 v65, v65, s69, v230
	v_med3_f32 v66, v66, s69, v230
	v_med3_f32 v67, v67, s69, v230
	v_pk_mul_f32 v[100:101], v[100:101], v[188:189]
	v_pk_mul_f32 v[102:103], v[102:103], v[190:191]
	v_pk_mul_f32 v[96:97], v[96:97], v[196:197]
	v_pk_mul_f32 v[98:99], v[98:99], v[198:199]
	v_pk_mul_f32 v[100:101], v[100:101], v[68:69]
	v_pk_mul_f32 v[102:103], v[102:103], v[70:71]
	v_pk_mul_f32 v[96:97], v[96:97], v[64:65]
	v_pk_mul_f32 v[98:99], v[98:99], v[66:67]
	v_cvt_pk_fp8_f32 v192, v100, v101
	v_cvt_pk_fp8_f32 v193, v96, v97
	v_cvt_pk_fp8_f32 v192, v102, v103 op_sel:[0,0,1]
	v_cvt_pk_fp8_f32 v193, v98, v99 op_sel:[0,0,1]
	s_nop 1
	global_store_dwordx2 v181, v[192:193], s[40:41]
	s_add_u32 s40, s40, 0x8000
	s_addc_u32 s41, s41, 0
	v_pk_fma_f32 v[92:93], v[92:93], v[200:201], v[172:173] op_sel_hi:[1,0,1]
	v_pk_fma_f32 v[94:95], v[94:95], v[200:201], v[174:175] op_sel_hi:[1,0,1]
	v_pk_fma_f32 v[88:89], v[88:89], v[200:201], v[160:161] op_sel_hi:[1,0,1]
	v_pk_fma_f32 v[90:91], v[90:91], v[200:201], v[162:163] op_sel_hi:[1,0,1]
	v_min_f32_e32 v92, 0x40e00000, v92
	v_min_f32_e32 v93, 0x40e00000, v93
	v_min_f32_e32 v94, 0x40e00000, v94
	v_min_f32_e32 v95, 0x40e00000, v95
	v_min_f32_e32 v88, 0x40e00000, v88
	v_min_f32_e32 v89, 0x40e00000, v89
	v_min_f32_e32 v90, 0x40e00000, v90
	v_min_f32_e32 v91, 0x40e00000, v91
	v_pk_mul_f32 v[188:189], v[92:93], v[200:201] op_sel:[0,1] op_sel_hi:[1,1]
	v_pk_mul_f32 v[190:191], v[94:95], v[200:201] op_sel:[0,1] op_sel_hi:[1,1]
	v_pk_mul_f32 v[196:197], v[88:89], v[200:201] op_sel:[0,1] op_sel_hi:[1,1]
	v_pk_mul_f32 v[198:199], v[90:91], v[200:201] op_sel:[0,1] op_sel_hi:[1,1]
	v_exp_f32_e32 v188, v188
	v_exp_f32_e32 v189, v189
	v_exp_f32_e32 v190, v190
	v_exp_f32_e32 v191, v191
	v_exp_f32_e32 v196, v196
	v_exp_f32_e32 v197, v197
	v_exp_f32_e32 v198, v198
	v_exp_f32_e32 v199, v199
	v_pk_fma_f32 v[60:61], v[60:61], v[200:201], v[168:169] op_sel_hi:[1,0,1]
	v_pk_fma_f32 v[62:63], v[62:63], v[200:201], v[170:171] op_sel_hi:[1,0,1]
	v_pk_fma_f32 v[56:57], v[56:57], v[200:201], v[164:165] op_sel_hi:[1,0,1]
	v_pk_fma_f32 v[58:59], v[58:59], v[200:201], v[166:167] op_sel_hi:[1,0,1]
	v_pk_add_f32 v[188:189], v[188:189], 1.0 op_sel_hi:[1,0]
	v_pk_add_f32 v[190:191], v[190:191], 1.0 op_sel_hi:[1,0]
	v_pk_add_f32 v[196:197], v[196:197], 1.0 op_sel_hi:[1,0]
	v_pk_add_f32 v[198:199], v[198:199], 1.0 op_sel_hi:[1,0]
	v_rcp_f32_e32 v188, v188
	v_rcp_f32_e32 v189, v189
	v_rcp_f32_e32 v190, v190
	v_rcp_f32_e32 v191, v191
	v_rcp_f32_e32 v196, v196
	v_rcp_f32_e32 v197, v197
	v_rcp_f32_e32 v198, v198
	v_rcp_f32_e32 v199, v199
	v_med3_f32 v60, v60, s69, v230
	v_med3_f32 v61, v61, s69, v230
	v_med3_f32 v62, v62, s69, v230
	v_med3_f32 v63, v63, s69, v230
	v_med3_f32 v56, v56, s69, v230
	v_med3_f32 v57, v57, s69, v230
	v_med3_f32 v58, v58, s69, v230
	v_med3_f32 v59, v59, s69, v230
	v_pk_mul_f32 v[92:93], v[92:93], v[188:189]
	v_pk_mul_f32 v[94:95], v[94:95], v[190:191]
	v_pk_mul_f32 v[88:89], v[88:89], v[196:197]
	v_pk_mul_f32 v[90:91], v[90:91], v[198:199]
	v_pk_mul_f32 v[92:93], v[92:93], v[60:61]
	v_pk_mul_f32 v[94:95], v[94:95], v[62:63]
	v_pk_mul_f32 v[88:89], v[88:89], v[56:57]
	v_pk_mul_f32 v[90:91], v[90:91], v[58:59]
	v_cvt_pk_fp8_f32 v192, v92, v93
	v_cvt_pk_fp8_f32 v193, v88, v89
	v_cvt_pk_fp8_f32 v192, v94, v95 op_sel:[0,0,1]
	v_cvt_pk_fp8_f32 v193, v90, v91 op_sel:[0,0,1]
	s_nop 1
	global_store_dwordx2 v181, v[192:193], s[40:41]
	s_add_u32 s40, s40, 0x8000
	s_addc_u32 s41, s41, 0
	v_pk_fma_f32 v[84:85], v[84:85], v[200:201], v[172:173] op_sel_hi:[1,0,1]
	v_pk_fma_f32 v[86:87], v[86:87], v[200:201], v[174:175] op_sel_hi:[1,0,1]
	v_pk_fma_f32 v[80:81], v[80:81], v[200:201], v[160:161] op_sel_hi:[1,0,1]
	v_pk_fma_f32 v[82:83], v[82:83], v[200:201], v[162:163] op_sel_hi:[1,0,1]
	v_min_f32_e32 v84, 0x40e00000, v84
	v_min_f32_e32 v85, 0x40e00000, v85
	v_min_f32_e32 v86, 0x40e00000, v86
	v_min_f32_e32 v87, 0x40e00000, v87
	v_min_f32_e32 v80, 0x40e00000, v80
	v_min_f32_e32 v81, 0x40e00000, v81
	v_min_f32_e32 v82, 0x40e00000, v82
	v_min_f32_e32 v83, 0x40e00000, v83
	v_pk_mul_f32 v[188:189], v[84:85], v[200:201] op_sel:[0,1] op_sel_hi:[1,1]
	v_pk_mul_f32 v[190:191], v[86:87], v[200:201] op_sel:[0,1] op_sel_hi:[1,1]
	v_pk_mul_f32 v[196:197], v[80:81], v[200:201] op_sel:[0,1] op_sel_hi:[1,1]
	v_pk_mul_f32 v[198:199], v[82:83], v[200:201] op_sel:[0,1] op_sel_hi:[1,1]
	v_exp_f32_e32 v188, v188
	v_exp_f32_e32 v189, v189
	v_exp_f32_e32 v190, v190
	v_exp_f32_e32 v191, v191
	v_exp_f32_e32 v196, v196
	v_exp_f32_e32 v197, v197
	v_exp_f32_e32 v198, v198
	v_exp_f32_e32 v199, v199
	v_pk_fma_f32 v[52:53], v[52:53], v[200:201], v[168:169] op_sel_hi:[1,0,1]
	v_pk_fma_f32 v[54:55], v[54:55], v[200:201], v[170:171] op_sel_hi:[1,0,1]
	v_pk_fma_f32 v[48:49], v[48:49], v[200:201], v[164:165] op_sel_hi:[1,0,1]
	v_pk_fma_f32 v[50:51], v[50:51], v[200:201], v[166:167] op_sel_hi:[1,0,1]
	v_pk_add_f32 v[188:189], v[188:189], 1.0 op_sel_hi:[1,0]
	v_pk_add_f32 v[190:191], v[190:191], 1.0 op_sel_hi:[1,0]
	v_pk_add_f32 v[196:197], v[196:197], 1.0 op_sel_hi:[1,0]
	v_pk_add_f32 v[198:199], v[198:199], 1.0 op_sel_hi:[1,0]
	v_rcp_f32_e32 v188, v188
	v_rcp_f32_e32 v189, v189
	v_rcp_f32_e32 v190, v190
	v_rcp_f32_e32 v191, v191
	v_rcp_f32_e32 v196, v196
	v_rcp_f32_e32 v197, v197
	v_rcp_f32_e32 v198, v198
	v_rcp_f32_e32 v199, v199
	v_med3_f32 v52, v52, s69, v230
	v_med3_f32 v53, v53, s69, v230
	v_med3_f32 v54, v54, s69, v230
	v_med3_f32 v55, v55, s69, v230
	v_med3_f32 v48, v48, s69, v230
	v_med3_f32 v49, v49, s69, v230
	v_med3_f32 v50, v50, s69, v230
	v_med3_f32 v51, v51, s69, v230
	v_pk_mul_f32 v[84:85], v[84:85], v[188:189]
	v_pk_mul_f32 v[86:87], v[86:87], v[190:191]
	v_pk_mul_f32 v[80:81], v[80:81], v[196:197]
	v_pk_mul_f32 v[82:83], v[82:83], v[198:199]
	v_pk_mul_f32 v[84:85], v[84:85], v[52:53]
	v_pk_mul_f32 v[86:87], v[86:87], v[54:55]
	v_pk_mul_f32 v[80:81], v[80:81], v[48:49]
	v_pk_mul_f32 v[82:83], v[82:83], v[50:51]
	v_cvt_pk_fp8_f32 v192, v84, v85
	v_cvt_pk_fp8_f32 v193, v80, v81
	v_cvt_pk_fp8_f32 v192, v86, v87 op_sel:[0,0,1]
	v_cvt_pk_fp8_f32 v193, v82, v83 op_sel:[0,0,1]
	s_nop 1
	global_store_dwordx2 v181, v[192:193], s[40:41]
	s_add_u32 s40, s40, 0x8000
	s_addc_u32 s41, s41, 0
	v_pk_fma_f32 v[76:77], v[76:77], v[200:201], v[172:173] op_sel_hi:[1,0,1]
	v_pk_fma_f32 v[78:79], v[78:79], v[200:201], v[174:175] op_sel_hi:[1,0,1]
	v_pk_fma_f32 v[72:73], v[72:73], v[200:201], v[160:161] op_sel_hi:[1,0,1]
	v_pk_fma_f32 v[74:75], v[74:75], v[200:201], v[162:163] op_sel_hi:[1,0,1]
	v_min_f32_e32 v76, 0x40e00000, v76
	v_min_f32_e32 v77, 0x40e00000, v77
	v_min_f32_e32 v78, 0x40e00000, v78
	v_min_f32_e32 v79, 0x40e00000, v79
	v_min_f32_e32 v72, 0x40e00000, v72
	v_min_f32_e32 v73, 0x40e00000, v73
	v_min_f32_e32 v74, 0x40e00000, v74
	v_min_f32_e32 v75, 0x40e00000, v75
	v_pk_mul_f32 v[188:189], v[76:77], v[200:201] op_sel:[0,1] op_sel_hi:[1,1]
	v_pk_mul_f32 v[190:191], v[78:79], v[200:201] op_sel:[0,1] op_sel_hi:[1,1]
	v_pk_mul_f32 v[196:197], v[72:73], v[200:201] op_sel:[0,1] op_sel_hi:[1,1]
	v_pk_mul_f32 v[198:199], v[74:75], v[200:201] op_sel:[0,1] op_sel_hi:[1,1]
	v_exp_f32_e32 v188, v188
	v_exp_f32_e32 v189, v189
	v_exp_f32_e32 v190, v190
	v_exp_f32_e32 v191, v191
	v_exp_f32_e32 v196, v196
	v_exp_f32_e32 v197, v197
	v_exp_f32_e32 v198, v198
	v_exp_f32_e32 v199, v199
	v_pk_fma_f32 v[40:41], v[40:41], v[200:201], v[168:169] op_sel_hi:[1,0,1]
	v_pk_fma_f32 v[42:43], v[42:43], v[200:201], v[170:171] op_sel_hi:[1,0,1]
	v_pk_fma_f32 v[32:33], v[32:33], v[200:201], v[164:165] op_sel_hi:[1,0,1]
	v_pk_fma_f32 v[34:35], v[34:35], v[200:201], v[166:167] op_sel_hi:[1,0,1]
	v_pk_add_f32 v[188:189], v[188:189], 1.0 op_sel_hi:[1,0]
	v_pk_add_f32 v[190:191], v[190:191], 1.0 op_sel_hi:[1,0]
	v_pk_add_f32 v[196:197], v[196:197], 1.0 op_sel_hi:[1,0]
	v_pk_add_f32 v[198:199], v[198:199], 1.0 op_sel_hi:[1,0]
	v_rcp_f32_e32 v188, v188
	v_rcp_f32_e32 v189, v189
	v_rcp_f32_e32 v190, v190
	v_rcp_f32_e32 v191, v191
	v_rcp_f32_e32 v196, v196
	v_rcp_f32_e32 v197, v197
	v_rcp_f32_e32 v198, v198
	v_rcp_f32_e32 v199, v199
	v_med3_f32 v40, v40, s69, v230
	v_med3_f32 v41, v41, s69, v230
	v_med3_f32 v42, v42, s69, v230
	v_med3_f32 v43, v43, s69, v230
	v_med3_f32 v32, v32, s69, v230
	v_med3_f32 v33, v33, s69, v230
	v_med3_f32 v34, v34, s69, v230
	v_med3_f32 v35, v35, s69, v230
	v_pk_mul_f32 v[76:77], v[76:77], v[188:189]
	v_pk_mul_f32 v[78:79], v[78:79], v[190:191]
	v_pk_mul_f32 v[72:73], v[72:73], v[196:197]
	v_pk_mul_f32 v[74:75], v[74:75], v[198:199]
	v_pk_mul_f32 v[76:77], v[76:77], v[40:41]
	v_pk_mul_f32 v[78:79], v[78:79], v[42:43]
	v_pk_mul_f32 v[72:73], v[72:73], v[32:33]
	v_pk_mul_f32 v[74:75], v[74:75], v[34:35]
	v_cvt_pk_fp8_f32 v192, v76, v77
	v_cvt_pk_fp8_f32 v193, v72, v73
	v_cvt_pk_fp8_f32 v192, v78, v79 op_sel:[0,0,1]
	v_cvt_pk_fp8_f32 v193, v74, v75 op_sel:[0,0,1]
	s_nop 1
	global_store_dwordx2 v181, v[192:193], s[40:41]
	s_add_u32 s40, s40, 0x28000
	s_addc_u32 s41, s41, 0
	v_pk_fma_f32 v[44:45], v[44:45], v[200:201], v[172:173] op_sel_hi:[1,0,1]
	v_pk_fma_f32 v[46:47], v[46:47], v[200:201], v[174:175] op_sel_hi:[1,0,1]
	v_pk_fma_f32 v[36:37], v[36:37], v[200:201], v[160:161] op_sel_hi:[1,0,1]
	v_pk_fma_f32 v[38:39], v[38:39], v[200:201], v[162:163] op_sel_hi:[1,0,1]
	v_min_f32_e32 v44, 0x40e00000, v44
	v_min_f32_e32 v45, 0x40e00000, v45
	v_min_f32_e32 v46, 0x40e00000, v46
	v_min_f32_e32 v47, 0x40e00000, v47
	v_min_f32_e32 v36, 0x40e00000, v36
	v_min_f32_e32 v37, 0x40e00000, v37
	v_min_f32_e32 v38, 0x40e00000, v38
	v_min_f32_e32 v39, 0x40e00000, v39
	v_pk_mul_f32 v[188:189], v[44:45], v[200:201] op_sel:[0,1] op_sel_hi:[1,1]
	v_pk_mul_f32 v[190:191], v[46:47], v[200:201] op_sel:[0,1] op_sel_hi:[1,1]
	v_pk_mul_f32 v[196:197], v[36:37], v[200:201] op_sel:[0,1] op_sel_hi:[1,1]
	v_pk_mul_f32 v[198:199], v[38:39], v[200:201] op_sel:[0,1] op_sel_hi:[1,1]
	v_exp_f32_e32 v188, v188
	v_exp_f32_e32 v189, v189
	v_exp_f32_e32 v190, v190
	v_exp_f32_e32 v191, v191
	v_exp_f32_e32 v196, v196
	v_exp_f32_e32 v197, v197
	v_exp_f32_e32 v198, v198
	v_exp_f32_e32 v199, v199
	v_pk_fma_f32 v[4:5], v[4:5], v[200:201], v[168:169] op_sel_hi:[1,0,1]
	v_pk_fma_f32 v[6:7], v[6:7], v[200:201], v[170:171] op_sel_hi:[1,0,1]
	v_pk_fma_f32 v[0:1], v[0:1], v[200:201], v[164:165] op_sel_hi:[1,0,1]
	v_pk_fma_f32 v[2:3], v[2:3], v[200:201], v[166:167] op_sel_hi:[1,0,1]
	v_pk_add_f32 v[188:189], v[188:189], 1.0 op_sel_hi:[1,0]
	v_pk_add_f32 v[190:191], v[190:191], 1.0 op_sel_hi:[1,0]
	v_pk_add_f32 v[196:197], v[196:197], 1.0 op_sel_hi:[1,0]
	v_pk_add_f32 v[198:199], v[198:199], 1.0 op_sel_hi:[1,0]
	v_rcp_f32_e32 v188, v188
	v_rcp_f32_e32 v189, v189
	v_rcp_f32_e32 v190, v190
	v_rcp_f32_e32 v191, v191
	v_rcp_f32_e32 v196, v196
	v_rcp_f32_e32 v197, v197
	v_rcp_f32_e32 v198, v198
	v_rcp_f32_e32 v199, v199
	v_med3_f32 v4, v4, s69, v230
	v_med3_f32 v5, v5, s69, v230
	v_med3_f32 v6, v6, s69, v230
	v_med3_f32 v7, v7, s69, v230
	v_med3_f32 v0, v0, s69, v230
	v_med3_f32 v1, v1, s69, v230
	v_med3_f32 v2, v2, s69, v230
	v_med3_f32 v3, v3, s69, v230
	v_pk_mul_f32 v[44:45], v[44:45], v[188:189]
	v_pk_mul_f32 v[46:47], v[46:47], v[190:191]
	v_pk_mul_f32 v[36:37], v[36:37], v[196:197]
	v_pk_mul_f32 v[38:39], v[38:39], v[198:199]
	v_pk_mul_f32 v[44:45], v[44:45], v[4:5]
	v_pk_mul_f32 v[46:47], v[46:47], v[6:7]
	v_pk_mul_f32 v[36:37], v[36:37], v[0:1]
	v_pk_mul_f32 v[38:39], v[38:39], v[2:3]
	v_cvt_pk_fp8_f32 v192, v44, v45
	v_cvt_pk_fp8_f32 v193, v36, v37
	v_cvt_pk_fp8_f32 v192, v46, v47 op_sel:[0,0,1]
	v_cvt_pk_fp8_f32 v193, v38, v39 op_sel:[0,0,1]
	s_nop 1
	global_store_dwordx2 v181, v[192:193], s[40:41]
	s_add_u32 s40, s40, 0x8000
	s_addc_u32 s41, s41, 0
	v_pk_fma_f32 v[28:29], v[28:29], v[200:201], v[172:173] op_sel_hi:[1,0,1]
	v_pk_fma_f32 v[30:31], v[30:31], v[200:201], v[174:175] op_sel_hi:[1,0,1]
	v_pk_fma_f32 v[24:25], v[24:25], v[200:201], v[160:161] op_sel_hi:[1,0,1]
	v_pk_fma_f32 v[26:27], v[26:27], v[200:201], v[162:163] op_sel_hi:[1,0,1]
	v_min_f32_e32 v28, 0x40e00000, v28
	v_min_f32_e32 v29, 0x40e00000, v29
	v_min_f32_e32 v30, 0x40e00000, v30
	v_min_f32_e32 v31, 0x40e00000, v31
	v_min_f32_e32 v24, 0x40e00000, v24
	v_min_f32_e32 v25, 0x40e00000, v25
	v_min_f32_e32 v26, 0x40e00000, v26
	v_min_f32_e32 v27, 0x40e00000, v27
	v_pk_mul_f32 v[188:189], v[28:29], v[200:201] op_sel:[0,1] op_sel_hi:[1,1]
	v_pk_mul_f32 v[190:191], v[30:31], v[200:201] op_sel:[0,1] op_sel_hi:[1,1]
	v_pk_mul_f32 v[196:197], v[24:25], v[200:201] op_sel:[0,1] op_sel_hi:[1,1]
	v_pk_mul_f32 v[198:199], v[26:27], v[200:201] op_sel:[0,1] op_sel_hi:[1,1]
	v_exp_f32_e32 v188, v188
	v_exp_f32_e32 v189, v189
	v_exp_f32_e32 v190, v190
	v_exp_f32_e32 v191, v191
	v_exp_f32_e32 v196, v196
	v_exp_f32_e32 v197, v197
	v_exp_f32_e32 v198, v198
	v_exp_f32_e32 v199, v199
	v_pk_fma_f32 v[104:105], v[104:105], v[200:201], v[168:169] op_sel_hi:[1,0,1]
	v_pk_fma_f32 v[106:107], v[106:107], v[200:201], v[170:171] op_sel_hi:[1,0,1]
	v_pk_fma_f32 v[108:109], v[108:109], v[200:201], v[164:165] op_sel_hi:[1,0,1]
	v_pk_fma_f32 v[110:111], v[110:111], v[200:201], v[166:167] op_sel_hi:[1,0,1]
	v_pk_add_f32 v[188:189], v[188:189], 1.0 op_sel_hi:[1,0]
	v_pk_add_f32 v[190:191], v[190:191], 1.0 op_sel_hi:[1,0]
	v_pk_add_f32 v[196:197], v[196:197], 1.0 op_sel_hi:[1,0]
	v_pk_add_f32 v[198:199], v[198:199], 1.0 op_sel_hi:[1,0]
	v_rcp_f32_e32 v188, v188
	v_rcp_f32_e32 v189, v189
	v_rcp_f32_e32 v190, v190
	v_rcp_f32_e32 v191, v191
	v_rcp_f32_e32 v196, v196
	v_rcp_f32_e32 v197, v197
	v_rcp_f32_e32 v198, v198
	v_rcp_f32_e32 v199, v199
	v_med3_f32 v104, v104, s69, v230
	v_med3_f32 v105, v105, s69, v230
	v_med3_f32 v106, v106, s69, v230
	v_med3_f32 v107, v107, s69, v230
	v_med3_f32 v108, v108, s69, v230
	v_med3_f32 v109, v109, s69, v230
	v_med3_f32 v110, v110, s69, v230
	v_med3_f32 v111, v111, s69, v230
	v_pk_mul_f32 v[28:29], v[28:29], v[188:189]
	v_pk_mul_f32 v[30:31], v[30:31], v[190:191]
	v_pk_mul_f32 v[24:25], v[24:25], v[196:197]
	v_pk_mul_f32 v[26:27], v[26:27], v[198:199]
	v_pk_mul_f32 v[28:29], v[28:29], v[104:105]
	v_pk_mul_f32 v[30:31], v[30:31], v[106:107]
	v_pk_mul_f32 v[24:25], v[24:25], v[108:109]
	v_pk_mul_f32 v[26:27], v[26:27], v[110:111]
	v_cvt_pk_fp8_f32 v192, v28, v29
	v_cvt_pk_fp8_f32 v193, v24, v25
	v_cvt_pk_fp8_f32 v192, v30, v31 op_sel:[0,0,1]
	v_cvt_pk_fp8_f32 v193, v26, v27 op_sel:[0,0,1]
	s_nop 1
	global_store_dwordx2 v181, v[192:193], s[40:41]
	s_add_u32 s40, s40, 0x8000
	s_addc_u32 s41, s41, 0
	v_pk_fma_f32 v[20:21], v[20:21], v[200:201], v[172:173] op_sel_hi:[1,0,1]
	v_pk_fma_f32 v[22:23], v[22:23], v[200:201], v[174:175] op_sel_hi:[1,0,1]
	v_pk_fma_f32 v[16:17], v[16:17], v[200:201], v[160:161] op_sel_hi:[1,0,1]
	v_pk_fma_f32 v[18:19], v[18:19], v[200:201], v[162:163] op_sel_hi:[1,0,1]
	v_min_f32_e32 v20, 0x40e00000, v20
	v_min_f32_e32 v21, 0x40e00000, v21
	v_min_f32_e32 v22, 0x40e00000, v22
	v_min_f32_e32 v23, 0x40e00000, v23
	v_min_f32_e32 v16, 0x40e00000, v16
	v_min_f32_e32 v17, 0x40e00000, v17
	v_min_f32_e32 v18, 0x40e00000, v18
	v_min_f32_e32 v19, 0x40e00000, v19
	v_pk_mul_f32 v[188:189], v[20:21], v[200:201] op_sel:[0,1] op_sel_hi:[1,1]
	v_pk_mul_f32 v[190:191], v[22:23], v[200:201] op_sel:[0,1] op_sel_hi:[1,1]
	v_pk_mul_f32 v[196:197], v[16:17], v[200:201] op_sel:[0,1] op_sel_hi:[1,1]
	v_pk_mul_f32 v[198:199], v[18:19], v[200:201] op_sel:[0,1] op_sel_hi:[1,1]
	v_exp_f32_e32 v188, v188
	v_exp_f32_e32 v189, v189
	v_exp_f32_e32 v190, v190
	v_exp_f32_e32 v191, v191
	v_exp_f32_e32 v196, v196
	v_exp_f32_e32 v197, v197
	v_exp_f32_e32 v198, v198
	v_exp_f32_e32 v199, v199
	v_pk_fma_f32 v[112:113], v[112:113], v[200:201], v[168:169] op_sel_hi:[1,0,1]
	v_pk_fma_f32 v[114:115], v[114:115], v[200:201], v[170:171] op_sel_hi:[1,0,1]
	v_pk_fma_f32 v[116:117], v[116:117], v[200:201], v[164:165] op_sel_hi:[1,0,1]
	v_pk_fma_f32 v[118:119], v[118:119], v[200:201], v[166:167] op_sel_hi:[1,0,1]
	v_pk_add_f32 v[188:189], v[188:189], 1.0 op_sel_hi:[1,0]
	v_pk_add_f32 v[190:191], v[190:191], 1.0 op_sel_hi:[1,0]
	v_pk_add_f32 v[196:197], v[196:197], 1.0 op_sel_hi:[1,0]
	v_pk_add_f32 v[198:199], v[198:199], 1.0 op_sel_hi:[1,0]
	v_rcp_f32_e32 v188, v188
	v_rcp_f32_e32 v189, v189
	v_rcp_f32_e32 v190, v190
	v_rcp_f32_e32 v191, v191
	v_rcp_f32_e32 v196, v196
	v_rcp_f32_e32 v197, v197
	v_rcp_f32_e32 v198, v198
	v_rcp_f32_e32 v199, v199
	v_med3_f32 v112, v112, s69, v230
	v_med3_f32 v113, v113, s69, v230
	v_med3_f32 v114, v114, s69, v230
	v_med3_f32 v115, v115, s69, v230
	v_med3_f32 v116, v116, s69, v230
	v_med3_f32 v117, v117, s69, v230
	v_med3_f32 v118, v118, s69, v230
	v_med3_f32 v119, v119, s69, v230
	v_pk_mul_f32 v[20:21], v[20:21], v[188:189]
	v_pk_mul_f32 v[22:23], v[22:23], v[190:191]
	v_pk_mul_f32 v[16:17], v[16:17], v[196:197]
	v_pk_mul_f32 v[18:19], v[18:19], v[198:199]
	v_pk_mul_f32 v[20:21], v[20:21], v[112:113]
	v_pk_mul_f32 v[22:23], v[22:23], v[114:115]
	v_pk_mul_f32 v[16:17], v[16:17], v[116:117]
	v_pk_mul_f32 v[18:19], v[18:19], v[118:119]
	v_cvt_pk_fp8_f32 v192, v20, v21
	v_cvt_pk_fp8_f32 v193, v16, v17
	v_cvt_pk_fp8_f32 v192, v22, v23 op_sel:[0,0,1]
	v_cvt_pk_fp8_f32 v193, v18, v19 op_sel:[0,0,1]
	s_nop 1
	global_store_dwordx2 v181, v[192:193], s[40:41]
	s_add_u32 s40, s40, 0x8000
	s_addc_u32 s41, s41, 0
	v_pk_fma_f32 v[12:13], v[12:13], v[200:201], v[172:173] op_sel_hi:[1,0,1]
	v_pk_fma_f32 v[14:15], v[14:15], v[200:201], v[174:175] op_sel_hi:[1,0,1]
	v_pk_fma_f32 v[8:9], v[8:9], v[200:201], v[160:161] op_sel_hi:[1,0,1]
	v_pk_fma_f32 v[10:11], v[10:11], v[200:201], v[162:163] op_sel_hi:[1,0,1]
	v_min_f32_e32 v12, 0x40e00000, v12
	v_min_f32_e32 v13, 0x40e00000, v13
	v_min_f32_e32 v14, 0x40e00000, v14
	v_min_f32_e32 v15, 0x40e00000, v15
	v_min_f32_e32 v8, 0x40e00000, v8
	v_min_f32_e32 v9, 0x40e00000, v9
	v_min_f32_e32 v10, 0x40e00000, v10
	v_min_f32_e32 v11, 0x40e00000, v11
	v_pk_mul_f32 v[188:189], v[12:13], v[200:201] op_sel:[0,1] op_sel_hi:[1,1]
	v_pk_mul_f32 v[190:191], v[14:15], v[200:201] op_sel:[0,1] op_sel_hi:[1,1]
	v_pk_mul_f32 v[196:197], v[8:9], v[200:201] op_sel:[0,1] op_sel_hi:[1,1]
	v_pk_mul_f32 v[198:199], v[10:11], v[200:201] op_sel:[0,1] op_sel_hi:[1,1]
	v_exp_f32_e32 v188, v188
	v_exp_f32_e32 v189, v189
	v_exp_f32_e32 v190, v190
	v_exp_f32_e32 v191, v191
	v_exp_f32_e32 v196, v196
	v_exp_f32_e32 v197, v197
	v_exp_f32_e32 v198, v198
	v_exp_f32_e32 v199, v199
	v_pk_fma_f32 v[120:121], v[120:121], v[200:201], v[168:169] op_sel_hi:[1,0,1]
	v_pk_fma_f32 v[122:123], v[122:123], v[200:201], v[170:171] op_sel_hi:[1,0,1]
	v_pk_fma_f32 v[124:125], v[124:125], v[200:201], v[164:165] op_sel_hi:[1,0,1]
	v_pk_fma_f32 v[126:127], v[126:127], v[200:201], v[166:167] op_sel_hi:[1,0,1]
	v_pk_add_f32 v[188:189], v[188:189], 1.0 op_sel_hi:[1,0]
	v_pk_add_f32 v[190:191], v[190:191], 1.0 op_sel_hi:[1,0]
	v_pk_add_f32 v[196:197], v[196:197], 1.0 op_sel_hi:[1,0]
	v_pk_add_f32 v[198:199], v[198:199], 1.0 op_sel_hi:[1,0]
	v_rcp_f32_e32 v188, v188
	v_rcp_f32_e32 v189, v189
	v_rcp_f32_e32 v190, v190
	v_rcp_f32_e32 v191, v191
	v_rcp_f32_e32 v196, v196
	v_rcp_f32_e32 v197, v197
	v_rcp_f32_e32 v198, v198
	v_rcp_f32_e32 v199, v199
	v_med3_f32 v120, v120, s69, v230
	v_med3_f32 v121, v121, s69, v230
	v_med3_f32 v122, v122, s69, v230
	v_med3_f32 v123, v123, s69, v230
	v_med3_f32 v124, v124, s69, v230
	v_med3_f32 v125, v125, s69, v230
	v_med3_f32 v126, v126, s69, v230
	v_med3_f32 v127, v127, s69, v230
	v_pk_mul_f32 v[12:13], v[12:13], v[188:189]
	v_pk_mul_f32 v[14:15], v[14:15], v[190:191]
	v_pk_mul_f32 v[8:9], v[8:9], v[196:197]
	v_pk_mul_f32 v[10:11], v[10:11], v[198:199]
	v_pk_mul_f32 v[12:13], v[12:13], v[120:121]
	v_pk_mul_f32 v[14:15], v[14:15], v[122:123]
	v_pk_mul_f32 v[8:9], v[8:9], v[124:125]
	v_pk_mul_f32 v[10:11], v[10:11], v[126:127]
	v_cvt_pk_fp8_f32 v192, v12, v13
	v_cvt_pk_fp8_f32 v193, v8, v9
	v_cvt_pk_fp8_f32 v192, v14, v15 op_sel:[0,0,1]
	v_cvt_pk_fp8_f32 v193, v10, v11 op_sel:[0,0,1]
	s_nop 1
	global_store_dwordx2 v181, v[192:193], s[40:41]
	s_nop 0
	s_mov_b64 s[40:41], s[100:101]
	s_waitcnt vmcnt(8)
	v_mul_f32_e32 v128, 0x43800000, v128
	v_mul_f32_e32 v132, 0x43800000, v132
	v_mov_b32_e32 v164, v177
	v_cvt_pk_fp8_f32 v164, v128, v132
	v_mul_f32_e32 v128, 0x43800000, v144
	v_mul_f32_e32 v132, 0x43800000, v148
	v_mov_b32_e32 v165, v177
	v_cvt_pk_fp8_f32 v165, v128, v132
	v_mul_f32_e32 v128, 0x43800000, v152
	v_mul_f32_e32 v132, 0x43800000, v156
	v_mul_f32_e32 v129, 0x43800000, v129
	v_cvt_pk_fp8_f32 v165, v128, v132 op_sel:[0,0,1]
	v_mul_f32_e32 v132, 0x43800000, v133
	v_mov_b32_e32 v128, v177
	v_mul_f32_e32 v133, 0x43800000, v137
	v_cvt_pk_fp8_f32 v128, v129, v132
	v_mul_f32_e32 v132, 0x43800000, v145
	v_mul_f32_e32 v137, 0x43800000, v149
	v_mov_b32_e32 v129, v177
	v_cvt_pk_fp8_f32 v129, v132, v137
	v_mul_f32_e32 v136, 0x43800000, v136
	v_mul_f32_e32 v140, 0x43800000, v140
	v_cvt_pk_fp8_f32 v164, v136, v140 op_sel:[0,0,1]
	v_mul_f32_e32 v136, 0x43800000, v141
	v_cvt_pk_fp8_f32 v128, v133, v136 op_sel:[0,0,1]
	v_mul_f32_e32 v132, 0x43800000, v153
	v_mul_f32_e32 v133, 0x43800000, v157
	v_cvt_pk_fp8_f32 v129, v132, v133 op_sel:[0,0,1]
	v_mul_f32_e32 v130, 0x43800000, v130
	v_mul_f32_e32 v133, 0x43800000, v134
	v_mov_b32_e32 v132, v177
	v_cvt_pk_fp8_f32 v132, v130, v133
	v_mul_f32_e32 v130, 0x43800000, v146
	v_mul_f32_e32 v137, 0x43800000, v150
	v_mov_b32_e32 v133, v177
	s_lshl_b32 s25, s38, 16
	s_mov_b64 s[38:39], s[42:43]
	v_cvt_pk_fp8_f32 v133, v130, v137
	v_mbcnt_lo_u32_b32 v160, -1, 0
	v_mbcnt_hi_u32_b32 v160, -1, v160
	s_mov_b64 s[38:39], s[100:101]
	v_mul_f32_e32 v134, 0x43800000, v138
	v_mul_f32_e32 v136, 0x43800000, v142
	v_cvt_pk_fp8_f32 v132, v134, v136 op_sel:[0,0,1]
	v_mul_f32_e32 v130, 0x43800000, v154
	v_mul_f32_e32 v134, 0x43800000, v158
	v_cvt_pk_fp8_f32 v133, v130, v134 op_sel:[0,0,1]
	v_mul_f32_e32 v131, 0x43800000, v131
	v_mul_f32_e32 v134, 0x43800000, v135
	v_mov_b32_e32 v130, v177
	v_cvt_pk_fp8_f32 v130, v131, v134
	v_mul_f32_e32 v134, 0x43800000, v147
	v_mul_f32_e32 v137, 0x43800000, v151
	v_mov_b32_e32 v131, v177
	s_and_b32 s25, s25, 0x3f0000
	s_lshl_b64 s[36:37], s[36:37], 22
	v_cvt_pk_fp8_f32 v131, v134, v137
	v_and_b32_e32 v161, -8, v160
	v_lshlrev_b32_e32 v160, 13, v160
	s_waitcnt lgkmcnt(0)
	s_add_u32 s36, s38, s36
	v_and_b32_e32 v160, 0xe000, v160
	s_addc_u32 s37, s39, s37
	s_or_b32 s7, s25, s7
	v_mul_f32_e32 v135, 0x43800000, v139
	v_mul_f32_e32 v136, 0x43800000, v143
	v_add3_u32 v160, s7, v161, v160
	v_mov_b32_e32 v161, v177
	v_cvt_pk_fp8_f32 v130, v135, v136 op_sel:[0,0,1]
	v_mul_f32_e32 v134, 0x43800000, v155
	v_mul_f32_e32 v135, 0x43800000, v159
	v_lshl_add_u64 v[160:161], s[36:37], 0, v[160:161]
	v_cvt_pk_fp8_f32 v131, v134, v135 op_sel:[0,0,1]
	v_lshl_add_u64 v[162:163], v[160:161], 0, s[22:23]
	v_add_co_u32_e32 v160, vcc, s70, v160
	s_nop 1
	v_addc_co_u32_e32 v161, vcc, 0, v161, vcc
	s_and_b64 vcc, exec, s[2:3]
	global_store_dwordx2 v[160:161], v[164:165], off offset:-4096
	global_store_dwordx2 v[162:163], v[128:129], off offset:2048
	global_store_dwordx2 v[160:161], v[132:133], off
	global_store_dwordx2 v[160:161], v[130:131], off offset:2048
	s_cbranch_vccnz .LBB0_920
	s_andn2_b64 vcc, exec, s[0:1]
	s_cbranch_vccnz .LBB0_919
	s_barrier
.LBB0_919:
	s_mov_b32 s48, s71
	s_mov_b32 s4, s24
	s_mov_b32 s6, s26
	s_andn2_b64 vcc, exec, s[28:29]
	s_cbranch_vccnz .LBB0_921
	s_branch .LBB0_922

.LBB0_996:
	s_mov_b32 s0, s26
	s_mov_b32 s4, s28
	s_mov_b32 s47, s62
	s_mov_b32 s60, s63
	s_andn2_b64 vcc, exec, s[30:31]
	s_mov_b64 s[38:39], s[34:35]
	s_cbranch_vccz .LBB0_1034
.LBB0_997:
	v_readlane_b32 s2, v254, 13
	v_readlane_b32 s3, v254, 14
	s_mov_b32 s2, s99
	s_add_i32 s63, s60, 1
	v_readlane_b32 s3, v254, 11
	s_waitcnt lgkmcnt(0)
	s_mul_i32 s2, s63, s2
	s_add_i32 s2, s2, s3
	s_cmp_lt_i32 s2, s25
	s_cselect_b64 s[36:37], -1, 0
	s_cmp_ge_i32 s2, s25
	s_cselect_b64 s[30:31], -1, 0
	s_and_b64 vcc, exec, s[30:31]
	s_cbranch_vccnz .LBB0_999
	s_and_b32 s3, s2, 7
	s_lshr_b32 s5, s2, 3
	s_lshl_b32 s27, s46, 0
	s_mul_i32 s3, s3, s27
	s_add_i32 s2, s3, s5
	s_lshr_b32 s3, s2, 6
	s_lshl_b32 s5, s3, 3
	s_and_b32 s2, s2, 63
	s_sub_i32 s27, s46, s5
	s_min_i32 s27, s27, 8
	v_mbcnt_lo_u32_b32 v131, -1, 0
	v_mbcnt_hi_u32_b32 v131, -1, v131
	v_lshlrev_b32_e32 v131, 2, v131
	v_add_u32_e32 v131, 0x24800, v131
	ds_read_b32 v133, v131
	s_cmp_eq_u32 s27, 8
	s_cbranch_scc0 .Lsched_slow_p7
	s_lshr_b32 s26, s2, 3
	s_and_b32 s2, s2, 7
	s_branch .Lsched_done_p7

.LBB0_999:
	v_cndmask_b32_e64 v131, 0, 1, s[36:37]
	v_cmp_ne_u32_e64 s[2:3], 1, v131
	s_andn2_b64 vcc, exec, s[36:37]
	s_mov_b64 s[34:35], s[38:39]
	s_cbranch_vccnz .LBB0_1001
	v_readlane_b32 s34, v254, 13
	v_readlane_b32 s35, v254, 14
	s_mov_b64 s[34:35], s[100:101]
	s_ashr_i32 s29, s28, 31
	s_lshl_b64 s[40:41], s[28:29], 22
	s_waitcnt lgkmcnt(0)
	s_add_u32 s5, s34, s40
	s_addc_u32 s29, s35, s41
	s_ashr_i32 s27, s26, 31
	s_lshl_b64 s[34:35], s[26:27], 19
	s_add_u32 s5, s5, s34
	s_addc_u32 s27, s29, s35
	s_add_u32 s34, s5, 0x22000000
	s_addc_u32 s35, s27, 0
.LBB0_1001:
	s_cmp_lt_i32 s60, 1
	s_cbranch_scc1 .LBB0_1008
	v_readlane_b32 s40, v254, 13
	v_readlane_b32 s41, v254, 14
	s_andn2_b64 vcc, exec, s[8:9]
	v_mbcnt_lo_u32_b32 v131, -1, 0
	v_mbcnt_hi_u32_b32 v131, -1, v131
	s_cbranch_vccnz .LBB0_1008
	s_mov_b64 s[44:45], -1
	s_and_b64 vcc, exec, s[18:19]
	s_cbranch_vccz .LBB0_1005
	s_mov_b64 s[42:43], s[100:101]
	s_waitcnt lgkmcnt(0)
	s_add_u32 s27, s42, s55
	s_addc_u32 s29, s43, 0
	s_lshl_b32 s42, s47, 8
	s_ashr_i32 s5, s4, 31
	s_ashr_i32 s43, s42, 31
	s_lshl_b64 s[44:45], s[4:5], 17
	s_lshl_b64 s[42:43], s[42:43], 2
	s_add_u32 s5, s27, s44
	s_addc_u32 s27, s29, s45
	s_add_u32 s42, s5, s42
	s_addc_u32 s43, s27, s43
	s_mov_b64 s[44:45], 0

.LBB0_1008:
	s_add_u32 s5, s38, 0x100
	s_addc_u32 s27, s39, 0
	s_lshl_b32 s44, s61, 8
	s_lshl_b32 s29, s61, 19
	s_bitset1_b32 s44, 7
	s_mov_b32 s45, -2
	s_mov_b64 s[38:39], 0
	s_cmp_eq_u32 s45, 12
	s_cselect_b64 s[42:43], -1, 0
	s_and_b64 s[40:41], s[36:37], s[42:43]
	s_andn2_b64 vcc, exec, s[40:41]
	v_mov_b32_e32 v131, v138
	v_mov_b32_e32 v133, v128
	v_add_u32_e32 v135, s58, v142
	s_add_u32 s64, s6, s38
	v_add_u32_e32 v137, s58, v143
	ds_read_b128 v[178:181], v135
	ds_read_b128 v[186:189], v135 offset:2048
	ds_read_b128 v[182:185], v137
	ds_read_b128 v[190:193], v137 offset:2048
	v_add_u32_e32 v135, s59, v142
	s_addc_u32 s65, s7, s39
	v_add_u32_e32 v137, s59, v143
	ds_read_b128 v[194:197], v135
	ds_read_b128 v[202:205], v135 offset:2048
	ds_read_b128 v[198:201], v137
	ds_read_b128 v[206:209], v137 offset:2048
	s_add_u32 s66, s64, 0x5e000100
	s_addc_u32 s67, s65, 0
	s_and_b64 s[40:41], s[42:43], exec
	s_cselect_b32 s41, s11, s67
	s_cselect_b32 s40, s10, s66
	s_add_u32 s66, s5, s38
	s_addc_u32 s67, s27, s39
	s_and_b64 s[42:43], s[42:43], exec
	s_cselect_b32 s43, s35, s67
	s_cselect_b32 s42, s34, s66
	ds_read_b128 v[210:213], v175
	ds_read_b128 v[218:221], v175 offset:2048
	ds_read_b128 v[214:217], v176
	ds_read_b128 v[222:225], v176 offset:2048
	ds_read_b128 v[226:229], v175 offset:4096
	ds_read_b128 v[234:237], v175 offset:6144
	ds_read_b128 v[230:233], v176 offset:4096
	ds_read_b128 v[238:241], v176 offset:6144
	s_add_i32 m0, s1, 0xc000
	v_lshl_add_u64 v[140:141], s[64:65], 0, v[128:129]
	v_lshl_add_u64 v[140:141], v[140:141], 0, s[16:17]
	global_load_lds_dwordx4 v[140:141], off
	v_mov_b32_e32 v139, v129
	v_lshl_add_u64 v[138:139], s[64:65], 0, v[138:139]
	v_lshl_add_u64 v[138:139], v[138:139], 0, s[16:17]
	s_add_i32 m0, s1, 0xe000
	s_nop 0
	global_load_lds_dwordx4 v[138:139], off
	s_waitcnt vmcnt(8)
	s_waitcnt lgkmcnt(0)
	s_barrier
	s_setprio 1
	s_waitcnt lgkmcnt(0)
	v_mfma_scale_f32_16x16x128_f8f6f4 v[100:103], v[178:185], v[210:217], 0, v177, v177 op_sel_hi:[0,0,0]
	v_mfma_scale_f32_16x16x128_f8f6f4 v[96:99], v[186:193], v[210:217], 0, v177, v177 op_sel_hi:[0,0,0]
	v_mfma_scale_f32_16x16x128_f8f6f4 v[92:95], v[178:185], v[218:225], 0, v177, v177 op_sel_hi:[0,0,0]
	v_mfma_scale_f32_16x16x128_f8f6f4 v[88:91], v[186:193], v[218:225], 0, v177, v177 op_sel_hi:[0,0,0]
	v_mfma_scale_f32_16x16x128_f8f6f4 v[84:87], v[178:185], v[226:233], 0, v177, v177 op_sel_hi:[0,0,0]
	v_mfma_scale_f32_16x16x128_f8f6f4 v[80:83], v[186:193], v[226:233], 0, v177, v177 op_sel_hi:[0,0,0]
	v_mfma_scale_f32_16x16x128_f8f6f4 v[242:245], v[178:185], v[234:241], 0, v177, v177 op_sel_hi:[0,0,0]
	v_mfma_scale_f32_16x16x128_f8f6f4 v[246:249], v[186:193], v[234:241], 0, v177, v177 op_sel_hi:[0,0,0]
	s_setprio 0
	s_setprio 1
	v_mfma_scale_f32_16x16x128_f8f6f4 v[40:43], v[194:201], v[234:241], 0, v177, v177 op_sel_hi:[0,0,0]
	v_mfma_scale_f32_16x16x128_f8f6f4 v[32:35], v[202:209], v[234:241], 0, v177, v177 op_sel_hi:[0,0,0]
	v_mfma_scale_f32_16x16x128_f8f6f4 v[250:253], v[194:201], v[210:217], 0, v177, v177 op_sel_hi:[0,0,0]
	v_mfma_scale_f32_16x16x128_f8f6f4 v[144:147], v[202:209], v[210:217], 0, v177, v177 op_sel_hi:[0,0,0]
	v_mfma_scale_f32_16x16x128_f8f6f4 v[148:151], v[194:201], v[218:225], 0, v177, v177 op_sel_hi:[0,0,0]
	v_mfma_scale_f32_16x16x128_f8f6f4 v[152:155], v[202:209], v[218:225], 0, v177, v177 op_sel_hi:[0,0,0]
	v_mfma_scale_f32_16x16x128_f8f6f4 v[156:159], v[194:201], v[226:233], 0, v177, v177 op_sel_hi:[0,0,0]
	v_mfma_scale_f32_16x16x128_f8f6f4 v[160:163], v[202:209], v[226:233], 0, v177, v177 op_sel_hi:[0,0,0]
	s_setprio 0
	s_barrier
	s_add_i32 s64, s58, s48
	s_mov_b32 m0, s64
	s_nop 2
	ds_read_b128 v[48:51], v175 offset:16384
	ds_read_b128 v[56:59], v175 offset:18432
	ds_read_b128 v[52:55], v176 offset:16384
	ds_read_b128 v[60:63], v176 offset:18432
	ds_read_b128 v[64:67], v175 offset:20480
	ds_read_b128 v[72:75], v175 offset:22528
	ds_read_b128 v[68:71], v176 offset:20480
	ds_read_b128 v[76:79], v176 offset:22528
	s_nop 0
	global_load_lds_dwordx4 v136, s[42:43]
	s_add_i32 m0, s64, 0x2000
	s_add_u32 s64, s42, 0x4000
	s_addc_u32 s65, s43, 0
	s_add_i32 s66, s59, s48
	s_nop 0
	global_load_lds_dwordx4 v130, s[42:43]
	s_mov_b32 m0, s66
	s_nop 0
	global_load_lds_dwordx4 v136, s[64:65]
	s_add_i32 m0, s66, 0x2000
	s_nop 0
	global_load_lds_dwordx4 v130, s[64:65]
	s_mov_b32 m0, s1
	s_nop 0
	global_load_lds_dwordx4 v132, s[40:41]
	s_mov_b32 m0, s49
	s_nop 0
	global_load_lds_dwordx4 v134, s[40:41]
	s_waitcnt vmcnt(8)
	s_waitcnt lgkmcnt(0)
	s_barrier
	s_setprio 1
	s_waitcnt lgkmcnt(0)
	v_mfma_scale_f32_16x16x128_f8f6f4 v[44:47], v[178:185], v[48:55], 0, v177, v177 op_sel_hi:[0,0,0]
	v_mfma_scale_f32_16x16x128_f8f6f4 v[36:39], v[186:193], v[48:55], 0, v177, v177 op_sel_hi:[0,0,0]
	v_mfma_scale_f32_16x16x128_f8f6f4 v[28:31], v[178:185], v[56:63], 0, v177, v177 op_sel_hi:[0,0,0]
	v_mfma_scale_f32_16x16x128_f8f6f4 v[24:27], v[186:193], v[56:63], 0, v177, v177 op_sel_hi:[0,0,0]
	v_mfma_scale_f32_16x16x128_f8f6f4 v[20:23], v[178:185], v[64:71], 0, v177, v177 op_sel_hi:[0,0,0]
	v_mfma_scale_f32_16x16x128_f8f6f4 v[16:19], v[186:193], v[64:71], 0, v177, v177 op_sel_hi:[0,0,0]
	v_mfma_scale_f32_16x16x128_f8f6f4 v[12:15], v[178:185], v[72:79], 0, v177, v177 op_sel_hi:[0,0,0]
	v_mfma_scale_f32_16x16x128_f8f6f4 v[8:11], v[186:193], v[72:79], 0, v177, v177 op_sel_hi:[0,0,0]
	s_setprio 0
	s_setprio 1
	v_mfma_scale_f32_16x16x128_f8f6f4 v[4:7], v[194:201], v[48:55], 0, v177, v177 op_sel_hi:[0,0,0]
	v_mfma_scale_f32_16x16x128_f8f6f4 v[0:3], v[202:209], v[48:55], 0, v177, v177 op_sel_hi:[0,0,0]
	v_mfma_scale_f32_16x16x128_f8f6f4 v[104:107], v[194:201], v[56:63], 0, v177, v177 op_sel_hi:[0,0,0]
	v_mfma_scale_f32_16x16x128_f8f6f4 v[108:111], v[202:209], v[56:63], 0, v177, v177 op_sel_hi:[0,0,0]
	v_mfma_scale_f32_16x16x128_f8f6f4 v[112:115], v[194:201], v[64:71], 0, v177, v177 op_sel_hi:[0,0,0]
	v_mfma_scale_f32_16x16x128_f8f6f4 v[116:119], v[202:209], v[64:71], 0, v177, v177 op_sel_hi:[0,0,0]
	v_mfma_scale_f32_16x16x128_f8f6f4 v[120:123], v[194:201], v[72:79], 0, v177, v177 op_sel_hi:[0,0,0]
	v_mfma_scale_f32_16x16x128_f8f6f4 v[124:127], v[202:209], v[72:79], 0, v177, v177 op_sel_hi:[0,0,0]
	s_setprio 0
	s_barrier
	s_add_i32 s64, 0, 0x18000
	v_add_u32_e32 v48, s64, v142
	s_add_i32 s65, 0, 0x1c000
	v_add_u32_e32 v49, s64, v143
	ds_read_b128 v[178:181], v48
	ds_read_b128 v[186:189], v48 offset:2048
	ds_read_b128 v[182:185], v49
	ds_read_b128 v[190:193], v49 offset:2048
	v_add_u32_e32 v48, s65, v142
	v_add_u32_e32 v49, s65, v143
	ds_read_b128 v[194:197], v48
	ds_read_b128 v[202:205], v48 offset:2048
	ds_read_b128 v[198:201], v49
	ds_read_b128 v[206:209], v49 offset:2048
	s_mov_b32 m0, s50
	v_mov_b32_e32 v128, v133
	ds_read_b128 v[48:51], v175 offset:32768
	ds_read_b128 v[210:213], v175 offset:34816
	ds_read_b128 v[52:55], v176 offset:32768
	ds_read_b128 v[214:217], v176 offset:34816
	ds_read_b128 v[218:221], v175 offset:36864
	ds_read_b128 v[226:229], v175 offset:38912
	ds_read_b128 v[222:225], v176 offset:36864
	ds_read_b128 v[230:233], v176 offset:38912
	v_mov_b32_e32 v138, v131
	global_load_lds_dwordx4 v128, s[40:41]
	s_mov_b32 m0, s51
	s_nop 0
	global_load_lds_dwordx4 v138, s[40:41]
	s_waitcnt vmcnt(8)
	s_waitcnt lgkmcnt(0)
	s_barrier
	s_setprio 1
	s_waitcnt lgkmcnt(0)
	v_mfma_scale_f32_16x16x128_f8f6f4 v[100:103], v[178:185], v[48:55], v[100:103], v177, v177 op_sel_hi:[0,0,0]
	v_mfma_scale_f32_16x16x128_f8f6f4 v[96:99], v[186:193], v[48:55], v[96:99], v177, v177 op_sel_hi:[0,0,0]
	v_mfma_scale_f32_16x16x128_f8f6f4 v[92:95], v[178:185], v[210:217], v[92:95], v177, v177 op_sel_hi:[0,0,0]
	v_mfma_scale_f32_16x16x128_f8f6f4 v[88:91], v[186:193], v[210:217], v[88:91], v177, v177 op_sel_hi:[0,0,0]
	v_mfma_scale_f32_16x16x128_f8f6f4 v[84:87], v[178:185], v[218:225], v[84:87], v177, v177 op_sel_hi:[0,0,0]
	v_mfma_scale_f32_16x16x128_f8f6f4 v[80:83], v[186:193], v[218:225], v[80:83], v177, v177 op_sel_hi:[0,0,0]
	v_mfma_scale_f32_16x16x128_f8f6f4 v[76:79], v[178:185], v[226:233], v[242:245], v177, v177 op_sel_hi:[0,0,0]
	v_mfma_scale_f32_16x16x128_f8f6f4 v[72:75], v[186:193], v[226:233], v[246:249], v177, v177 op_sel_hi:[0,0,0]
	s_setprio 0
	s_setprio 1
	v_mfma_scale_f32_16x16x128_f8f6f4 v[68:71], v[194:201], v[48:55], v[250:253], v177, v177 op_sel_hi:[0,0,0]
	v_mfma_scale_f32_16x16x128_f8f6f4 v[64:67], v[202:209], v[48:55], v[144:147], v177, v177 op_sel_hi:[0,0,0]
	v_mfma_scale_f32_16x16x128_f8f6f4 v[60:63], v[194:201], v[210:217], v[148:151], v177, v177 op_sel_hi:[0,0,0]
	v_mfma_scale_f32_16x16x128_f8f6f4 v[56:59], v[202:209], v[210:217], v[152:155], v177, v177 op_sel_hi:[0,0,0]
	v_mfma_scale_f32_16x16x128_f8f6f4 v[52:55], v[194:201], v[218:225], v[156:159], v177, v177 op_sel_hi:[0,0,0]
	v_mfma_scale_f32_16x16x128_f8f6f4 v[48:51], v[202:209], v[218:225], v[160:163], v177, v177 op_sel_hi:[0,0,0]
	v_mfma_scale_f32_16x16x128_f8f6f4 v[40:43], v[194:201], v[226:233], v[40:43], v177, v177 op_sel_hi:[0,0,0]
	v_mfma_scale_f32_16x16x128_f8f6f4 v[32:35], v[202:209], v[226:233], v[32:35], v177, v177 op_sel_hi:[0,0,0]
	s_setprio 0
	s_barrier
	v_mov_b32_e32 v137, v129
	ds_read_b128 v[210:213], v175 offset:49152
	ds_read_b128 v[218:221], v175 offset:51200
	ds_read_b128 v[214:217], v176 offset:49152
	ds_read_b128 v[222:225], v176 offset:51200
	ds_read_b128 v[226:229], v175 offset:53248
	ds_read_b128 v[234:237], v175 offset:55296
	ds_read_b128 v[230:233], v176 offset:53248
	ds_read_b128 v[238:241], v176 offset:55296
	s_add_i32 s64, s64, s48
	v_lshl_add_u64 v[140:141], s[42:43], 0, v[136:137]
	v_lshl_add_u64 v[140:141], v[140:141], 0, s[14:15]
	s_mov_b32 m0, s64
	v_mov_b32_e32 v131, v129
	global_load_lds_dwordx4 v[140:141], off
	s_add_i32 m0, s64, 0x2000
	v_mov_b32_e32 v133, v129
	v_lshl_add_u64 v[140:141], s[42:43], 0, v[130:131]
	s_add_u32 s42, s42, 0x4080
	v_lshl_add_u64 v[140:141], v[140:141], 0, s[14:15]
	s_addc_u32 s43, s43, 0
	s_add_i32 s64, s65, s48
	global_load_lds_dwordx4 v[140:141], off
	s_mov_b32 m0, s64
	v_mov_b32_e32 v135, v129
	global_load_lds_dwordx4 v136, s[42:43]
	s_add_i32 m0, s64, 0x2000
	s_nop 0
	global_load_lds_dwordx4 v130, s[42:43]
	s_mov_b32 m0, s53
	v_lshl_add_u64 v[140:141], s[40:41], 0, v[132:133]
	v_lshl_add_u64 v[140:141], v[140:141], 0, s[14:15]
	global_load_lds_dwordx4 v[140:141], off
	s_mov_b32 m0, s54
	v_lshl_add_u64 v[140:141], s[40:41], 0, v[134:135]
	v_lshl_add_u64 v[140:141], v[140:141], 0, s[14:15]
	global_load_lds_dwordx4 v[140:141], off
	s_waitcnt vmcnt(8)
	s_waitcnt lgkmcnt(0)
	s_barrier
	s_setprio 1
	s_waitcnt lgkmcnt(0)
	v_mfma_scale_f32_16x16x128_f8f6f4 v[44:47], v[178:185], v[210:217], v[44:47], v177, v177 op_sel_hi:[0,0,0]
	v_mfma_scale_f32_16x16x128_f8f6f4 v[36:39], v[186:193], v[210:217], v[36:39], v177, v177 op_sel_hi:[0,0,0]
	v_mfma_scale_f32_16x16x128_f8f6f4 v[28:31], v[178:185], v[218:225], v[28:31], v177, v177 op_sel_hi:[0,0,0]
	v_mfma_scale_f32_16x16x128_f8f6f4 v[24:27], v[186:193], v[218:225], v[24:27], v177, v177 op_sel_hi:[0,0,0]
	v_mfma_scale_f32_16x16x128_f8f6f4 v[20:23], v[178:185], v[226:233], v[20:23], v177, v177 op_sel_hi:[0,0,0]
	v_mfma_scale_f32_16x16x128_f8f6f4 v[16:19], v[186:193], v[226:233], v[16:19], v177, v177 op_sel_hi:[0,0,0]
	v_mfma_scale_f32_16x16x128_f8f6f4 v[12:15], v[178:185], v[234:241], v[12:15], v177, v177 op_sel_hi:[0,0,0]
	v_mfma_scale_f32_16x16x128_f8f6f4 v[8:11], v[186:193], v[234:241], v[8:11], v177, v177 op_sel_hi:[0,0,0]
	s_setprio 0
	s_setprio 1
	v_mfma_scale_f32_16x16x128_f8f6f4 v[4:7], v[194:201], v[210:217], v[4:7], v177, v177 op_sel_hi:[0,0,0]
	v_mfma_scale_f32_16x16x128_f8f6f4 v[0:3], v[202:209], v[210:217], v[0:3], v177, v177 op_sel_hi:[0,0,0]
	v_mfma_scale_f32_16x16x128_f8f6f4 v[104:107], v[194:201], v[218:225], v[104:107], v177, v177 op_sel_hi:[0,0,0]
	v_mfma_scale_f32_16x16x128_f8f6f4 v[108:111], v[202:209], v[218:225], v[108:111], v177, v177 op_sel_hi:[0,0,0]
	v_mfma_scale_f32_16x16x128_f8f6f4 v[112:115], v[194:201], v[226:233], v[112:115], v177, v177 op_sel_hi:[0,0,0]
	v_mfma_scale_f32_16x16x128_f8f6f4 v[116:119], v[202:209], v[226:233], v[116:119], v177, v177 op_sel_hi:[0,0,0]
	v_mfma_scale_f32_16x16x128_f8f6f4 v[120:123], v[194:201], v[234:241], v[120:123], v177, v177 op_sel_hi:[0,0,0]
	v_mfma_scale_f32_16x16x128_f8f6f4 v[124:127], v[202:209], v[234:241], v[124:127], v177, v177 op_sel_hi:[0,0,0]
	s_setprio 0
	s_barrier
	s_add_i32 s45, s45, 2
	s_add_u32 s38, s38, 0x100
	s_addc_u32 s39, s39, 0
	s_branch .LBB0_1010

.LBB0_1014:
	s_bitcmp1_b32 s60, 0
	s_cselect_b32 s29, 0xc00, 0
	s_lshl_b32 s38, s56, 2
	s_or_b32 s38, s29, s38
	v_mbcnt_lo_u32_b32 v133, -1, 0
	v_mbcnt_hi_u32_b32 v133, -1, v133
	s_add_i32 s38, s38, 0x24c00
	v_and_b32_e32 v135, -16, v133
	v_lshl_add_u32 v131, v135, 2, s38
	s_or_b32 s38, s29, 0x25000
	s_add_i32 s39, s29, 0x25400
	s_lshl_b32 s29, s0, 8
	v_readlane_b32 s36, v254, 13
	s_or_b32 s29, s29, s56
	v_readlane_b32 s37, v254, 14
	v_add_u32_e32 v140, s29, v135
	s_lshl_b32 s29, s4, 2
	s_add_i32 s29, s29, 0x248a0
	s_mov_b64 s[36:37], s[100:101]
	v_mov_b32_e32 v135, s29
	ds_read_b32 v135, v135
	v_and_or_b32 v178, v133, 15, s52
	v_ashrrev_i32_e32 v141, 31, v140
	s_lshl_b32 s29, s47, 8
	s_waitcnt lgkmcnt(0)
	v_lshl_add_u64 v[140:141], s[36:37], 0, v[140:141]
	v_add_u32_e32 v139, s29, v178
	v_lshlrev_b32_e32 v137, 2, v178
	v_lshl_add_u64 v[140:141], v[140:141], 0, s[22:23]
	v_cmp_lt_i32_e32 vcc, v139, v135
	v_add_u32_e32 v133, s38, v137
	v_add_u32_e32 v137, s39, v137
	s_and_saveexec_b64 s[36:37], vcc
	s_cbranch_execz .LBB0_1016
	ds_read_b32 v152, v137
	ds_read_b32 v160, v133
	ds_read_b128 v[144:147], v131
	ds_read_b128 v[148:151], v131 offset:16
	s_waitcnt lgkmcnt(0)
	v_mul_f32_e32 v162, 0x41000000, v152
	ds_read_b128 v[152:155], v131 offset:32
	ds_read_b128 v[156:159], v131 offset:48
	v_pk_fma_f32 v[144:145], v[100:101], s[24:25], v[144:145] op_sel_hi:[1,0,1]
	v_pk_fma_f32 v[146:147], v[102:103], s[24:25], v[146:147] op_sel_hi:[1,0,1]
	v_pk_mul_f32 v[180:181], v[144:145], v[162:163] op_sel_hi:[1,0]
	v_pk_fma_f32 v[144:145], v[96:97], s[24:25], v[148:149] op_sel_hi:[1,0,1]
	v_pk_mul_f32 v[146:147], v[146:147], v[162:163] op_sel_hi:[1,0]
	v_pk_mul_f32 v[148:149], v[162:163], v[144:145] op_sel_hi:[0,1]
	v_mov_b32_e32 v144, v129
	v_cvt_pk_fp8_f32 v144, v180, v181
	v_mov_b32_e32 v145, v129
	v_cvt_pk_fp8_f32 v145, v148, v149
	v_pk_fma_f32 v[148:149], v[98:99], s[24:25], v[150:151] op_sel_hi:[1,0,1]
	v_cvt_pk_fp8_f32 v144, v146, v147 op_sel:[0,0,1]
	v_pk_mul_f32 v[148:149], v[162:163], v[148:149] op_sel_hi:[0,1]
	s_waitcnt lgkmcnt(0)
	v_pk_fma_f32 v[146:147], v[70:71], s[24:25], v[154:155] op_sel_hi:[1,0,1]
	v_cvt_pk_fp8_f32 v145, v148, v149 op_sel:[0,0,1]
	v_pk_fma_f32 v[148:149], v[68:69], s[24:25], v[152:153] op_sel_hi:[1,0,1]
	v_pk_mul_f32 v[150:151], v[162:163], v[146:147] op_sel_hi:[0,1]
	v_pk_fma_f32 v[146:147], v[64:65], s[24:25], v[156:157] op_sel_hi:[1,0,1]
	v_pk_mul_f32 v[148:149], v[162:163], v[148:149] op_sel_hi:[0,1]
	v_pk_mul_f32 v[152:153], v[162:163], v[146:147] op_sel_hi:[0,1]
	v_mov_b32_e32 v146, v129
	v_mov_b32_e32 v147, v129
	v_cvt_pk_fp8_f32 v146, v148, v149
	v_cvt_pk_fp8_f32 v147, v152, v153
	v_pk_fma_f32 v[148:149], v[66:67], s[24:25], v[158:159] op_sel_hi:[1,0,1]
	v_ashrrev_i32_e32 v161, 31, v160
	v_pk_mul_f32 v[148:149], v[162:163], v[148:149] op_sel_hi:[0,1]
	v_cvt_pk_fp8_f32 v146, v150, v151 op_sel:[0,0,1]
	v_cvt_pk_fp8_f32 v147, v148, v149 op_sel:[0,0,1]
	v_lshlrev_b64 v[148:149], 11, v[160:161]
	v_lshl_add_u64 v[148:149], v[140:141], 0, v[148:149]
	global_store_dwordx4 v[148:149], v[144:147], off

	.amdhsa_kernel _Z6mk_fwd4Args
		.amdhsa_group_segment_fixed_size 0
		.amdhsa_private_segment_fixed_size 0
		.amdhsa_kernarg_size 464
		.amdhsa_user_sgpr_count 2
		.amdhsa_user_sgpr_dispatch_ptr 0
		.amdhsa_user_sgpr_queue_ptr 0
		.amdhsa_user_sgpr_kernarg_segment_ptr 1
		.amdhsa_user_sgpr_dispatch_id 0
		.amdhsa_user_sgpr_kernarg_preload_length 0
		.amdhsa_user_sgpr_kernarg_preload_offset 0
		.amdhsa_user_sgpr_private_segment_size 0
		.amdhsa_uses_dynamic_stack 0
		.amdhsa_enable_private_segment 0
		.amdhsa_system_sgpr_workgroup_id_x 1
		.amdhsa_system_sgpr_workgroup_id_y 0
		.amdhsa_system_sgpr_workgroup_id_z 0
		.amdhsa_system_sgpr_workgroup_info 0
		.amdhsa_system_vgpr_workitem_id 0
		.amdhsa_next_free_vgpr 256
		.amdhsa_next_free_sgpr 102
		.amdhsa_accum_offset 256
		.amdhsa_reserve_vcc 1
		.amdhsa_float_round_mode_32 0
		.amdhsa_float_round_mode_16_64 0
		.amdhsa_float_denorm_mode_32 3
		.amdhsa_float_denorm_mode_16_64 3
		.amdhsa_dx10_clamp 1
		.amdhsa_ieee_mode 1
		.amdhsa_fp16_overflow 0
		.amdhsa_tg_split 0
		.amdhsa_exception_fp_ieee_invalid_op 0
		.amdhsa_exception_fp_denorm_src 0
		.amdhsa_exception_fp_ieee_div_zero 0
		.amdhsa_exception_fp_ieee_overflow 0
		.amdhsa_exception_fp_ieee_underflow 0
		.amdhsa_exception_fp_ieee_inexact 0
		.amdhsa_exception_int_div_zero 0
	.end_amdhsa_kernel

amdhsa.kernels:
  - .agpr_count:     0
    .args:
      - .offset:         0
        .size:           208
        .value_kind:     by_value
      - .offset:         208
        .size:           4
        .value_kind:     hidden_block_count_x
      - .offset:         212
        .size:           4
        .value_kind:     hidden_block_count_y
      - .offset:         216
        .size:           4
        .value_kind:     hidden_block_count_z
      - .offset:         220
        .size:           2
        .value_kind:     hidden_group_size_x
      - .offset:         222
        .size:           2
        .value_kind:     hidden_group_size_y
      - .offset:         224
        .size:           2
        .value_kind:     hidden_group_size_z
      - .offset:         226
        .size:           2
        .value_kind:     hidden_remainder_x
      - .offset:         228
        .size:           2
        .value_kind:     hidden_remainder_y
      - .offset:         230
        .size:           2
        .value_kind:     hidden_remainder_z
      - .offset:         248
        .size:           8
        .value_kind:     hidden_global_offset_x
      - .offset:         256
        .size:           8
        .value_kind:     hidden_global_offset_y
      - .offset:         264
        .size:           8
        .value_kind:     hidden_global_offset_z
      - .offset:         272
        .size:           2
        .value_kind:     hidden_grid_dims
      - .offset:         328
        .size:           4
        .value_kind:     hidden_dynamic_lds_size
    .group_segment_fixed_size: 0
    .kernarg_segment_align: 8
    .kernarg_segment_size: 464
    .language:       OpenCL C
    .language_version:
      - 2
      - 0
    .max_flat_workgroup_size: 512
    .name:           _Z6mk_fwd4Args
    .private_segment_fixed_size: 0
    .sgpr_count:     108
    .sgpr_spill_count: 125
    .symbol:         _Z6mk_fwd4Args.kd
    .uniform_work_group_size: 1
    .uses_dynamic_stack: false
    .vgpr_count:     256
    .vgpr_spill_count: 0
    .wavefront_size: 64
